# speedup vs baseline: 1.1148x; 1.0198x over previous
.LBB5_96:
	s_andn2_b64 vcc, exec, s[4:5]
	s_cbranch_vccnz .LBB5_143
	s_setprio 3
	s_load_dwordx2 s[8:9], s[0:1], 0x0
	s_load_dwordx2 s[10:11], s[0:1], 0x8
	s_load_dwordx2 s[12:13], s[0:1], 0x18
	s_load_dwordx2 s[32:33], s[0:1], 0x28
	s_load_dwordx4 s[36:39], s[0:1], 0x30
	s_load_dwordx2 s[18:19], s[0:1], 0xb8
	s_load_dwordx2 s[16:17], s[0:1], 0xc8
	s_load_dword s34, s[0:1], 0xd4
	s_lshr_b32 s3, s2, 4
	s_bfe_u32 s4, s2, 0x10003
	s_and_b32 s5, s2, 7
	v_lshrrev_b32_e32 v1, 6, v0
	v_and_b32_e32 v2, 63, v0
	v_and_b32_e32 v3, 15, v0
	v_bfe_u32 v4, v0, 4, 2
	s_nop 1
	v_readfirstlane_b32 s6, v1
	s_waitcnt lgkmcnt(0)
	s_cmp_eq_u32 s3, 0
	s_cselect_b32 s12, s12, s32
	s_cselect_b32 s13, s13, s33
	s_cselect_b32 s14, s36, s38
	s_cselect_b32 s15, s37, s39
	s_mul_i32 s35, s4, 0x708
	s_add_u32 s12, s12, s35
	s_addc_u32 s13, s13, 0
	s_mul_i32 s35, s5, 0x25800
	s_add_u32 s14, s14, s35
	s_addc_u32 s15, s15, 0
	s_mul_i32 s35, s4, 0x258
	s_add_u32 s14, s14, s35
	s_addc_u32 s15, s15, 0
	s_lshl_b64 s[10:11], s[10:11], 2
	s_mul_i32 s35, s3, 0x384000
	s_add_u32 s8, s8, s35
	s_addc_u32 s9, s9, 0
	s_mul_i32 s35, s5, 0x70800
	s_add_u32 s8, s8, s35
	s_addc_u32 s9, s9, 0
	s_mul_i32 s35, s4, 0x708
	s_add_u32 s8, s8, s35
	s_addc_u32 s9, s9, 0
	s_mul_i32 s35, s4, 112
	s_lshl_b32 s40, s6, 1
	s_add_i32 s35, s35, s40
	s_mul_i32 s35, s35, 0xe10
	s_add_u32 s22, s8, s35
	s_addc_u32 s23, s9, 0
	s_add_u32 s46, s22, 0xe10
	s_addc_u32 s47, s23, 0
	s_cmp_eq_u32 s4, 0
	s_mov_b32 s27, 0xffff1f00
	s_mov_b32 s20, 0xfffffb50
	s_cselect_b32 s27, 0xe100, s27
	s_cselect_b32 s50, 0, -1
	s_cselect_b32 s20, 0x4b0, s20
	s_cselect_b32 s21, 0, -1
	s_lshl_b32 s35, s3, 1
	s_add_i32 s35, s35, s4
	s_add_i32 s35, s35, s34
	s_mul_i32 s35, s35, 0x28000
	s_add_u32 s16, s16, s35
	s_addc_u32 s17, s17, 0
	s_mul_i32 s35, s6, 0x5000
	s_add_u32 s16, s16, s35
	s_addc_u32 s17, s17, 0
	s_mov_b32 s28, 0xffff
	s_mov_b32 s29, 0
	s_mov_b32 s30, -1
	s_mov_b32 s31, 1
	s_mov_b32 s68, 0x00330033
	s_mov_b32 s69, 0x00330033
	s_mov_b32 s51, 0xbfb8aa3b
	s_mov_b32 s52, 0x4038aa3b
	v_lshlrev_b32_e32 v5, 4, v2
	v_mov_b32_e32 v36, 0
	v_mov_b32_e32 v37, 0
	v_mov_b32_e32 v38, 0
	v_mov_b32_e32 v39, 0
	v_mov_b32_e32 v60, 0
	v_mov_b32_e32 v61, 0
	v_mov_b32_e32 v62, 0
	v_mov_b32_e32 v63, 0
	v_mov_b32_e32 v84, 0
	v_mov_b32_e32 v85, 0
	v_mov_b32_e32 v86, 0
	v_mov_b32_e32 v87, 0
	v_mov_b32_e32 v108, 0
	v_mov_b32_e32 v109, 0
	v_mov_b32_e32 v110, 0
	v_mov_b32_e32 v111, 0
	s_add_u32 s42, s16, 0x0
	s_addc_u32 s43, s17, 0
	global_load_dwordx4 v[16:19], v5, s[42:43] offset:0
	global_load_dwordx4 v[20:23], v5, s[42:43] offset:1024
	global_load_dwordx4 v[24:27], v5, s[42:43] offset:2048
	global_load_dwordx4 v[28:31], v5, s[42:43] offset:3072
	s_add_u32 s42, s16, 0x1000
	s_addc_u32 s43, s17, 0
	global_load_dwordx4 v[32:35], v5, s[42:43]
	s_add_u32 s42, s16, 0x1400
	s_addc_u32 s43, s17, 0
	global_load_dwordx4 v[40:43], v5, s[42:43] offset:0
	global_load_dwordx4 v[44:47], v5, s[42:43] offset:1024
	global_load_dwordx4 v[48:51], v5, s[42:43] offset:2048
	global_load_dwordx4 v[52:55], v5, s[42:43] offset:3072
	s_add_u32 s42, s16, 0x2400
	s_addc_u32 s43, s17, 0
	global_load_dwordx4 v[56:59], v5, s[42:43]
	s_add_u32 s42, s16, 0x2800
	s_addc_u32 s43, s17, 0
	global_load_dwordx4 v[64:67], v5, s[42:43] offset:0
	global_load_dwordx4 v[68:71], v5, s[42:43] offset:1024
	global_load_dwordx4 v[72:75], v5, s[42:43] offset:2048
	global_load_dwordx4 v[76:79], v5, s[42:43] offset:3072
	s_add_u32 s42, s16, 0x3800
	s_addc_u32 s43, s17, 0
	global_load_dwordx4 v[80:83], v5, s[42:43]
	s_add_u32 s42, s16, 0x3c00
	s_addc_u32 s43, s17, 0
	global_load_dwordx4 v[88:91], v5, s[42:43] offset:0
	global_load_dwordx4 v[92:95], v5, s[42:43] offset:1024
	global_load_dwordx4 v[96:99], v5, s[42:43] offset:2048
	global_load_dwordx4 v[100:103], v5, s[42:43] offset:3072
	s_add_u32 s42, s16, 0x4c00
	s_addc_u32 s43, s17, 0
	global_load_dwordx4 v[104:107], v5, s[42:43]
	v_lshlrev_b32_e32 v172, 3, v2
	v_min_u32_e32 v6, 32, v2
	v_lshlrev_b32_e32 v114, 3, v6
	global_load_dwordx2 v[176:177], v172, s[22:23] offset:0
	global_load_dwordx2 v[178:179], v172, s[22:23] offset:512
	global_load_dwordx2 v[180:181], v172, s[22:23] offset:1024
	global_load_dwordx2 v[182:183], v114, s[22:23] offset:1536
	global_load_dwordx2 v[184:185], v172, s[46:47] offset:0
	global_load_dwordx2 v[186:187], v172, s[46:47] offset:512
	global_load_dwordx2 v[188:189], v172, s[46:47] offset:1024
	global_load_dwordx2 v[190:191], v114, s[46:47] offset:1536
	v_and_b32_e32 v6, 1, v3
	v_cmp_eq_u32_e32 vcc, 1, v6
	v_mov_b32_e32 v7, 0x44444444
	v_mov_b32_e32 v8, 0xeeeeeeee
	s_nop 1
	v_cndmask_b32_e32 v112, v7, v8, vcc
	s_mul_i32 s53, s6, 19
	v_add_u32_e32 v6, s53, v3
	v_cmp_gt_u32_e32 vcc, 0x96, v6
	v_add_u32_e32 v7, 0x12c, v6
	v_mov_b32_e32 v8, 0x12c
	s_nop 1
	v_cndmask_b32_e32 v7, v8, v7, vcc
	v_lshlrev_b32_e32 v7, 2, v7
	global_load_dword v9, v7, s[12:13]
	s_mov_b64 s[54:55], vcc
	v_cmp_gt_u32_e32 vcc, 0xc0, v0
	v_lshlrev_b32_e32 v10, 2, v0
	v_mov_b32_e32 v11, 0
	s_and_saveexec_b64 s[44:45], vcc
	ds_write_b32 v10, v11 offset:61440
	s_mov_b64 exec, s[44:45]
	v_and_b32_e32 v10, 31, v0
	v_lshrrev_b32_e32 v11, 5, v0
	v_subrev_u32_e32 v12, 6, v10
	v_max_i32_e32 v12, 0, v12
	v_mul_u32_u24_e32 v13, 11, v12
	v_lshrrev_b32_e32 v13, 5, v13
	v_mul_u32_u24_e32 v14, 3, v13
	v_sub_u32_e32 v14, v12, v14
	v_mul_u32_u24_e32 v15, 19, v13
	v_add3_u32 v15, v15, v14, 16
	v_cmp_gt_u32_e32 vcc, 0x96, v15
	v_cmp_lt_u32_e64 s[56:57], 5, v10
	v_cmp_gt_u32_e64 s[58:59], 30, v10
	s_and_b64 s[56:57], s[56:57], vcc
	s_and_b64 s[56:57], s[56:57], s[58:59]
	v_add_u32_e32 v15, 0x12c, v15
	v_mov_b32_e32 v14, 0x12c
	v_cndmask_b32_e64 v15, v14, v15, s[56:57]
	v_lshlrev_b32_e32 v15, 2, v15
	global_load_dword v14, v15, s[12:13]
	v_mul_u32_u24_e32 v11, 0x780, v11
	v_lshl_add_u32 v11, v10, 2, v11
	s_waitcnt vmcnt(0)
	v_mul_f32_e32 v14, s52, v14
	v_mul_f32_e32 v9, s52, v9
	v_cndmask_b32_e64 v14, 0, v14, s[56:57]
	v_cndmask_b32_e64 v113, 0, v9, s[54:55]
	s_and_saveexec_b64 s[44:45], s[58:59]
	ds_write_b32 v11, v14 offset:1800
	ds_write_b32 v11, v14 offset:32520
	s_mov_b64 exec, s[44:45]
	v_lshlrev_b32_e32 v172, 3, v2
	s_lshl_b32 s35, s6, 1
	s_sub_i32 s40, 15, s35
	s_cmp_eq_u32 s4, 0
	s_cselect_b32 s41, s35, s40
	s_add_i32 s35, s35, 1
	s_sub_i32 s40, 15, s35
	s_cmp_eq_u32 s4, 0
	s_cselect_b32 s40, s35, s40
	s_mul_i32 s41, s41, 0x780
	s_mul_i32 s40, s40, 0x780
	v_add_u32_e32 v173, s41, v172
	v_add_u32_e32 v174, s40, v172
	v_min_u32_e32 v6, 32, v2
	v_lshlrev_b32_e32 v114, 3, v6
	v_add_u32_e32 v115, s41, v114
	v_add_u32_e32 v169, s40, v114
	v_cmp_lt_u32_e32 vcc, 21, v2
	v_mov_b32_e32 v6, s51
	v_mov_b32_e32 v7, s52
	s_nop 0
	v_cndmask_b32_e32 v175, v6, v7, vcc
	s_waitcnt vmcnt(0)
	v_mul_f32_e32 v176, s51, v176
	v_mul_f32_e32 v177, s51, v177
	v_mul_f32_e32 v178, s51, v178
	v_mul_f32_e32 v179, s51, v179
	v_mul_f32_e32 v180, v175, v180
	v_mul_f32_e32 v181, v175, v181
	v_mul_f32_e32 v182, s52, v182
	v_mul_f32_e32 v183, s52, v183
	ds_write_b64 v173, v[176:177] offset:0
	ds_write_b64 v173, v[178:179] offset:512
	ds_write_b64 v173, v[180:181] offset:1024
	ds_write_b64 v115, v[182:183] offset:1536
	v_mul_f32_e32 v184, s51, v184
	v_mul_f32_e32 v185, s51, v185
	v_mul_f32_e32 v186, s51, v186
	v_mul_f32_e32 v187, s51, v187
	v_mul_f32_e32 v188, v175, v188
	v_mul_f32_e32 v189, v175, v189
	v_mul_f32_e32 v190, s52, v190
	v_mul_f32_e32 v191, s52, v191
	ds_write_b64 v174, v[184:185] offset:0
	ds_write_b64 v174, v[186:187] offset:512
	ds_write_b64 v174, v[188:189] offset:1024
	ds_write_b64 v169, v[190:191] offset:1536
	s_movk_i32 s55, 0x7800
	v_add_u32_e32 v173, s55, v173
	v_add_u32_e32 v174, s55, v174
	v_add_u32_e32 v115, s55, v115
	v_add_u32_e32 v169, s55, v169
	s_sub_i32 s55, 0, s55
	v_add_u32_e32 v6, s53, v2
	v_cmp_gt_u32_e32 vcc, 0x96, v6
	v_cmp_gt_u32_e64 s[56:57], 16, v2
	v_cmp_gt_u32_e64 s[58:59], 19, v2
	s_and_b64 s[56:57], s[56:57], vcc
	s_and_b64 s[58:59], s[58:59], vcc
	v_mov_b32_e32 v7, 0x710
	v_lshlrev_b32_e32 v8, 2, v6
	v_add_u32_e32 v9, 0x258, v8
	v_add_u32_e32 v10, 0x4b0, v8
	v_cndmask_b32_e64 v163, v7, v8, s[56:57]
	v_cndmask_b32_e64 v164, v7, v9, s[56:57]
	v_cndmask_b32_e64 v166, v7, v10, s[58:59]
	v_subrev_u32_e32 v9, 16, v2
	v_cmp_gt_u32_e64 s[60:61], 6, v9
	v_cmp_lt_u32_e32 vcc, 2, v9
	v_mov_b32_e32 v11, 0x93
	s_nop 0
	v_cndmask_b32_e32 v10, 0, v11, vcc
	v_cndmask_b32_e64 v12, 0, 3, vcc
	v_sub_u32_e32 v13, v6, v12
	v_cmp_gt_u32_e32 vcc, 0x96, v13
	s_and_b64 s[60:61], s[60:61], vcc
	v_add_u32_e32 v13, v6, v10
	v_lshlrev_b32_e32 v13, 2, v13
	v_cndmask_b32_e64 v165, v7, v13, s[60:61]
	v_subrev_u32_e32 v9, 22, v2
	v_cmp_gt_u32_e32 vcc, 3, v9
	s_mul_i32 s35, s6, 3
	s_addk_i32 s35, 0x1c8
	v_add_lshl_u32 v9, v9, s35, 2
	s_nop 0
	v_cndmask_b32_e32 v165, v165, v9, vcc
	v_and_b32_e32 v9, 1, v3
	v_lshlrev_b32_e32 v9, 4, v9
	v_lshl_or_b32 v9, v4, 5, v9
	v_add_u32_e32 v167, 0xf000, v9
	v_and_b32_e32 v9, 0xfffffff0, v6
	v_bfe_u32 v10, v6, 1, 1
	v_lshl_or_b32 v9, v10, 3, v9
	v_bfe_u32 v10, v6, 2, 2
	v_lshl_or_b32 v9, v10, 1, v9
	v_and_b32_e32 v10, 1, v6
	v_or_b32_e32 v9, v9, v10
	v_lshlrev_b32_e32 v9, 1, v9
	v_add_u32_e32 v9, 0xf000, v9
	v_lshlrev_b32_e32 v10, 1, v2
	v_add_u32_e32 v10, 0xf300, v10
	v_cndmask_b32_e64 v168, v10, v9, s[58:59]
	s_mul_i32 s35, s4, 0x25350
	s_add_u32 s14, s14, s35
	s_addc_u32 s15, s15, 0
	s_add_u32 s18, s18, 0x25800
	s_addc_u32 s19, s19, 0
	v_lshlrev_b32_e32 v9, 2, v0
	v_mov_b32_e32 v10, s18
	v_mov_b32_e32 v11, s19
	v_mov_b32_e32 v12, s14
	v_mov_b32_e32 v13, s15
	v_cndmask_b32_e64 v9, v9, v8, s[58:59]
	v_cndmask_b32_e64 v10, v10, v12, s[58:59]
	v_cndmask_b32_e64 v11, v11, v13, s[58:59]
	v_add_co_u32_e32 v170, vcc, v10, v9
	s_nop 1
	v_addc_co_u32_e32 v171, vcc, 0, v11, vcc
	v_mov_b32_e32 v161, 0
	v_mov_b32_e32 v137, 0
	v_mov_b32_e32 v138, 0
	v_mov_b32_e32 v139, 0
	v_mov_b32_e32 v141, 0
	v_mov_b32_e32 v142, 0
	v_mov_b32_e32 v143, 0
	v_mov_b32_e32 v145, 0
	v_mov_b32_e32 v146, 0
	v_mov_b32_e32 v147, 0
	v_mov_b32_e32 v149, 0
	v_mov_b32_e32 v150, 0
	v_mov_b32_e32 v151, 0
	s_mov_b32 s26, 0
	s_waitcnt vmcnt(0) lgkmcnt(0)
	s_barrier
	ds_read_b32 v136, v163 offset:0
	ds_read_b32 v140, v164 offset:0
	ds_read_b32 v148, v165 offset:0
	ds_read_b32 v152, v166 offset:0
	v_mov_b32_e32 v144, v113
	s_waitcnt lgkmcnt(0)
.Lgru1_chunk:
	ds_read_b128 v[116:119], v167 offset:0
	ds_read_b128 v[120:123], v167 offset:128
	ds_read_b128 v[124:127], v167 offset:256
	s_waitcnt lgkmcnt(2)
	v_smfmac_f32_16x16x64_f16 v[136:139], v[116:119], v[16:23], v112
	v_smfmac_f32_16x16x64_f16 v[148:151], v[116:119], v[88:95], v112
	s_waitcnt lgkmcnt(1)
	v_smfmac_f32_16x16x64_f16 v[136:139], v[120:123], v[24:31], v112
	v_smfmac_f32_16x16x64_f16 v[148:151], v[120:123], v[96:103], v112
	s_waitcnt lgkmcnt(0)
	v_smfmac_f32_16x16x64_f16 v[136:139], v[124:127], v[32:39], v112
	v_smfmac_f32_16x16x64_f16 v[148:151], v[124:127], v[104:111], v112
	v_smfmac_f32_16x16x64_f16 v[144:147], v[116:119], v[64:71], v112
	v_smfmac_f32_16x16x64_f16 v[140:143], v[116:119], v[40:47], v112
	v_smfmac_f32_16x16x64_f16 v[144:147], v[120:123], v[72:79], v112
	v_smfmac_f32_16x16x64_f16 v[140:143], v[120:123], v[48:55], v112
	s_nop 3
	v_add_f32_e32 v153, v136, v137
	v_add_f32_e32 v156, v148, v149
	v_smfmac_f32_16x16x64_f16 v[144:147], v[124:127], v[80:87], v112
	v_cndmask_b32_e64 v159, v156, v153, s[28:29]
	v_exp_f32_e32 v159, v159
	v_smfmac_f32_16x16x64_f16 v[140:143], v[124:127], v[56:63], v112
	v_mov_b32_dpp v157, v156 row_shl:3 row_mask:0xf bank_mask:0xf bound_ctrl:1
	v_mov_b32_dpp v158, v156 row_shl:6 row_mask:0xf bank_mask:0xf bound_ctrl:1
	v_add_f32_e32 v159, 1.0, v159
	v_rcp_f32_e32 v159, v159
	s_nop 0
	v_add_f32_e32 v155, v144, v145
	v_cndmask_b32_e64 v155, v158, v155, s[28:29]
	v_fmac_f32_e32 v152, v159, v155
	v_exp_f32_e32 v152, v152
	v_add_f32_e32 v154, v140, v141
	v_cndmask_b32_e64 v160, v157, v154, s[28:29]
	v_exp_f32_e32 v160, v160
	v_add_f32_e32 v152, 1.0, v152
	v_rcp_f32_e32 v159, v152
	v_add_f32_e32 v160, 1.0, v160
	v_rcp_f32_e32 v160, v160
	ds_read_b32 v136, v163 offset:1920
	ds_read_b32 v140, v164 offset:1920
	ds_read_b32 v148, v165 offset:1920
	v_mov_b32_e32 v144, v113
	v_fma_f32 v159, v159, -2.0, 1.0
	ds_read_b32 v152, v166 offset:1920
	v_sub_f32_e32 v153, v161, v159
	v_fma_mixlo_f16 v162, v160, v153, v159
	ds_write_b16 v168, v162 offset:384
	v_fma_f32 v161, v160, v153, v159
	v_mov_b32_e32 v137, 0
	v_mov_b32_e32 v141, 0
	v_mov_b32_e32 v145, 0
	v_mov_b32_e32 v149, 0
	global_store_dword v[170:171], v161, off
	v_lshl_add_u64 v[170:171], v[170:171], 0, s[20:21]
	s_waitcnt lgkmcnt(0)
	s_barrier
	ds_read_b128 v[116:119], v167 offset:384
	ds_read_b128 v[120:123], v167 offset:512
	ds_read_b128 v[124:127], v167 offset:640
	s_waitcnt lgkmcnt(2)
	v_smfmac_f32_16x16x64_f16 v[136:139], v[116:119], v[16:23], v112
	v_smfmac_f32_16x16x64_f16 v[148:151], v[116:119], v[88:95], v112
	s_waitcnt lgkmcnt(1)
	v_smfmac_f32_16x16x64_f16 v[136:139], v[120:123], v[24:31], v112
	v_smfmac_f32_16x16x64_f16 v[148:151], v[120:123], v[96:103], v112
	s_waitcnt lgkmcnt(0)
	v_smfmac_f32_16x16x64_f16 v[136:139], v[124:127], v[32:39], v112
	v_smfmac_f32_16x16x64_f16 v[148:151], v[124:127], v[104:111], v112
	s_cmp_eq_u32 s26, 7
	s_cbranch_scc1 .Lgru1_nopf
	s_add_u32 s22, s22, s27
	s_addc_u32 s23, s23, s50
	s_add_u32 s46, s46, s27
	s_addc_u32 s47, s47, s50
	global_load_dwordx2 v[176:177], v172, s[22:23] offset:0
	global_load_dwordx2 v[178:179], v172, s[22:23] offset:512
	global_load_dwordx2 v[180:181], v172, s[22:23] offset:1024
	global_load_dwordx2 v[184:185], v172, s[46:47] offset:0
	global_load_dwordx2 v[186:187], v172, s[46:47] offset:512
	global_load_dwordx2 v[188:189], v172, s[46:47] offset:1024
	global_load_dwordx2 v[182:183], v114, s[22:23] offset:1536
	global_load_dwordx2 v[190:191], v114, s[46:47] offset:1536
.Lgru1_nopf:
	v_smfmac_f32_16x16x64_f16 v[144:147], v[116:119], v[64:71], v112
	v_smfmac_f32_16x16x64_f16 v[140:143], v[116:119], v[40:47], v112
	v_smfmac_f32_16x16x64_f16 v[144:147], v[120:123], v[72:79], v112
	v_smfmac_f32_16x16x64_f16 v[140:143], v[120:123], v[48:55], v112
	s_nop 3
	v_add_f32_e32 v153, v136, v137
	v_add_f32_e32 v156, v148, v149
	v_smfmac_f32_16x16x64_f16 v[144:147], v[124:127], v[80:87], v112
	v_cndmask_b32_e64 v159, v156, v153, s[28:29]
	v_exp_f32_e32 v159, v159
	v_smfmac_f32_16x16x64_f16 v[140:143], v[124:127], v[56:63], v112
	v_mov_b32_dpp v157, v156 row_shl:3 row_mask:0xf bank_mask:0xf bound_ctrl:1
	v_mov_b32_dpp v158, v156 row_shl:6 row_mask:0xf bank_mask:0xf bound_ctrl:1
	v_add_f32_e32 v159, 1.0, v159
	v_rcp_f32_e32 v159, v159
	s_nop 0
	v_add_f32_e32 v155, v144, v145
	v_cndmask_b32_e64 v155, v158, v155, s[28:29]
	v_fmac_f32_e32 v152, v159, v155
	v_exp_f32_e32 v152, v152
	v_add_f32_e32 v154, v140, v141
	v_cndmask_b32_e64 v160, v157, v154, s[28:29]
	v_exp_f32_e32 v160, v160
	v_add_f32_e32 v152, 1.0, v152
	v_rcp_f32_e32 v159, v152
	v_add_f32_e32 v160, 1.0, v160
	v_rcp_f32_e32 v160, v160
	ds_read_b32 v136, v163 offset:3840
	ds_read_b32 v140, v164 offset:3840
	ds_read_b32 v148, v165 offset:3840
	v_mov_b32_e32 v144, v113
	v_fma_f32 v159, v159, -2.0, 1.0
	ds_read_b32 v152, v166 offset:3840
	v_sub_f32_e32 v153, v161, v159
	v_fma_mixlo_f16 v162, v160, v153, v159
	ds_write_b16 v168, v162 offset:0
	v_fma_f32 v161, v160, v153, v159
	v_mov_b32_e32 v137, 0
	v_mov_b32_e32 v141, 0
	v_mov_b32_e32 v145, 0
	v_mov_b32_e32 v149, 0
	global_store_dword v[170:171], v161, off
	v_lshl_add_u64 v[170:171], v[170:171], 0, s[20:21]
	s_waitcnt lgkmcnt(0)
	s_barrier
	ds_read_b128 v[116:119], v167 offset:0
	ds_read_b128 v[120:123], v167 offset:128
	ds_read_b128 v[124:127], v167 offset:256
	s_waitcnt lgkmcnt(2)
	v_smfmac_f32_16x16x64_f16 v[136:139], v[116:119], v[16:23], v112
	v_smfmac_f32_16x16x64_f16 v[148:151], v[116:119], v[88:95], v112
	s_waitcnt lgkmcnt(1)
	v_smfmac_f32_16x16x64_f16 v[136:139], v[120:123], v[24:31], v112
	v_smfmac_f32_16x16x64_f16 v[148:151], v[120:123], v[96:103], v112
	s_waitcnt lgkmcnt(0)
	v_smfmac_f32_16x16x64_f16 v[136:139], v[124:127], v[32:39], v112
	v_smfmac_f32_16x16x64_f16 v[148:151], v[124:127], v[104:111], v112
	v_smfmac_f32_16x16x64_f16 v[144:147], v[116:119], v[64:71], v112
	v_smfmac_f32_16x16x64_f16 v[140:143], v[116:119], v[40:47], v112
	v_smfmac_f32_16x16x64_f16 v[144:147], v[120:123], v[72:79], v112
	v_smfmac_f32_16x16x64_f16 v[140:143], v[120:123], v[48:55], v112
	s_nop 3
	v_add_f32_e32 v153, v136, v137
	v_add_f32_e32 v156, v148, v149
	v_smfmac_f32_16x16x64_f16 v[144:147], v[124:127], v[80:87], v112
	v_cndmask_b32_e64 v159, v156, v153, s[28:29]
	v_exp_f32_e32 v159, v159
	v_smfmac_f32_16x16x64_f16 v[140:143], v[124:127], v[56:63], v112
	v_mov_b32_dpp v157, v156 row_shl:3 row_mask:0xf bank_mask:0xf bound_ctrl:1
	v_mov_b32_dpp v158, v156 row_shl:6 row_mask:0xf bank_mask:0xf bound_ctrl:1
	v_add_f32_e32 v159, 1.0, v159
	v_rcp_f32_e32 v159, v159
	s_nop 0
	v_add_f32_e32 v155, v144, v145
	v_cndmask_b32_e64 v155, v158, v155, s[28:29]
	v_fmac_f32_e32 v152, v159, v155
	v_exp_f32_e32 v152, v152
	v_add_f32_e32 v154, v140, v141
	v_cndmask_b32_e64 v160, v157, v154, s[28:29]
	v_exp_f32_e32 v160, v160
	v_add_f32_e32 v152, 1.0, v152
	v_rcp_f32_e32 v159, v152
	v_add_f32_e32 v160, 1.0, v160
	v_rcp_f32_e32 v160, v160
	ds_read_b32 v136, v163 offset:5760
	ds_read_b32 v140, v164 offset:5760
	ds_read_b32 v148, v165 offset:5760
	v_mov_b32_e32 v144, v113
	v_fma_f32 v159, v159, -2.0, 1.0
	ds_read_b32 v152, v166 offset:5760
	v_sub_f32_e32 v153, v161, v159
	v_fma_mixlo_f16 v162, v160, v153, v159
	ds_write_b16 v168, v162 offset:384
	v_fma_f32 v161, v160, v153, v159
	v_mov_b32_e32 v137, 0
	v_mov_b32_e32 v141, 0
	v_mov_b32_e32 v145, 0
	v_mov_b32_e32 v149, 0
	global_store_dword v[170:171], v161, off
	v_lshl_add_u64 v[170:171], v[170:171], 0, s[20:21]
	s_waitcnt lgkmcnt(0)
	s_barrier
	ds_read_b128 v[116:119], v167 offset:384
	ds_read_b128 v[120:123], v167 offset:512
	ds_read_b128 v[124:127], v167 offset:640
	s_waitcnt lgkmcnt(2)
	v_smfmac_f32_16x16x64_f16 v[136:139], v[116:119], v[16:23], v112
	v_smfmac_f32_16x16x64_f16 v[148:151], v[116:119], v[88:95], v112
	s_waitcnt lgkmcnt(1)
	v_smfmac_f32_16x16x64_f16 v[136:139], v[120:123], v[24:31], v112
	v_smfmac_f32_16x16x64_f16 v[148:151], v[120:123], v[96:103], v112
	s_waitcnt lgkmcnt(0)
	v_smfmac_f32_16x16x64_f16 v[136:139], v[124:127], v[32:39], v112
	v_smfmac_f32_16x16x64_f16 v[148:151], v[124:127], v[104:111], v112
	v_smfmac_f32_16x16x64_f16 v[144:147], v[116:119], v[64:71], v112
	v_smfmac_f32_16x16x64_f16 v[140:143], v[116:119], v[40:47], v112
	v_smfmac_f32_16x16x64_f16 v[144:147], v[120:123], v[72:79], v112
	v_smfmac_f32_16x16x64_f16 v[140:143], v[120:123], v[48:55], v112
	s_nop 3
	v_add_f32_e32 v153, v136, v137
	v_add_f32_e32 v156, v148, v149
	v_smfmac_f32_16x16x64_f16 v[144:147], v[124:127], v[80:87], v112
	v_cndmask_b32_e64 v159, v156, v153, s[28:29]
	v_exp_f32_e32 v159, v159
	v_smfmac_f32_16x16x64_f16 v[140:143], v[124:127], v[56:63], v112
	v_mov_b32_dpp v157, v156 row_shl:3 row_mask:0xf bank_mask:0xf bound_ctrl:1
	v_mov_b32_dpp v158, v156 row_shl:6 row_mask:0xf bank_mask:0xf bound_ctrl:1
	v_add_f32_e32 v159, 1.0, v159
	v_rcp_f32_e32 v159, v159
	s_nop 0
	v_add_f32_e32 v155, v144, v145
	v_cndmask_b32_e64 v155, v158, v155, s[28:29]
	v_fmac_f32_e32 v152, v159, v155
	v_exp_f32_e32 v152, v152
	v_add_f32_e32 v154, v140, v141
	v_cndmask_b32_e64 v160, v157, v154, s[28:29]
	v_exp_f32_e32 v160, v160
	v_add_f32_e32 v152, 1.0, v152
	v_rcp_f32_e32 v159, v152
	v_add_f32_e32 v160, 1.0, v160
	v_rcp_f32_e32 v160, v160
	ds_read_b32 v136, v163 offset:7680
	ds_read_b32 v140, v164 offset:7680
	ds_read_b32 v148, v165 offset:7680
	v_mov_b32_e32 v144, v113
	v_fma_f32 v159, v159, -2.0, 1.0
	ds_read_b32 v152, v166 offset:7680
	v_sub_f32_e32 v153, v161, v159
	v_fma_mixlo_f16 v162, v160, v153, v159
	ds_write_b16 v168, v162 offset:0
	v_fma_f32 v161, v160, v153, v159
	v_mov_b32_e32 v137, 0
	v_mov_b32_e32 v141, 0
	v_mov_b32_e32 v145, 0
	v_mov_b32_e32 v149, 0
	global_store_dword v[170:171], v161, off
	v_lshl_add_u64 v[170:171], v[170:171], 0, s[20:21]
	s_waitcnt lgkmcnt(0)
	s_barrier
	ds_read_b128 v[116:119], v167 offset:0
	ds_read_b128 v[120:123], v167 offset:128
	ds_read_b128 v[124:127], v167 offset:256
	s_waitcnt lgkmcnt(2)
	v_smfmac_f32_16x16x64_f16 v[136:139], v[116:119], v[16:23], v112
	v_smfmac_f32_16x16x64_f16 v[148:151], v[116:119], v[88:95], v112
	s_waitcnt lgkmcnt(1)
	v_smfmac_f32_16x16x64_f16 v[136:139], v[120:123], v[24:31], v112
	v_smfmac_f32_16x16x64_f16 v[148:151], v[120:123], v[96:103], v112
	s_waitcnt lgkmcnt(0)
	v_smfmac_f32_16x16x64_f16 v[136:139], v[124:127], v[32:39], v112
	v_smfmac_f32_16x16x64_f16 v[148:151], v[124:127], v[104:111], v112
	v_smfmac_f32_16x16x64_f16 v[144:147], v[116:119], v[64:71], v112
	v_smfmac_f32_16x16x64_f16 v[140:143], v[116:119], v[40:47], v112
	v_smfmac_f32_16x16x64_f16 v[144:147], v[120:123], v[72:79], v112
	v_smfmac_f32_16x16x64_f16 v[140:143], v[120:123], v[48:55], v112
	s_nop 3
	v_add_f32_e32 v153, v136, v137
	v_add_f32_e32 v156, v148, v149
	v_smfmac_f32_16x16x64_f16 v[144:147], v[124:127], v[80:87], v112
	v_cndmask_b32_e64 v159, v156, v153, s[28:29]
	v_exp_f32_e32 v159, v159
	v_smfmac_f32_16x16x64_f16 v[140:143], v[124:127], v[56:63], v112
	v_mov_b32_dpp v157, v156 row_shl:3 row_mask:0xf bank_mask:0xf bound_ctrl:1
	v_mov_b32_dpp v158, v156 row_shl:6 row_mask:0xf bank_mask:0xf bound_ctrl:1
	v_add_f32_e32 v159, 1.0, v159
	v_rcp_f32_e32 v159, v159
	s_nop 0
	v_add_f32_e32 v155, v144, v145
	v_cndmask_b32_e64 v155, v158, v155, s[28:29]
	v_fmac_f32_e32 v152, v159, v155
	v_exp_f32_e32 v152, v152
	v_add_f32_e32 v154, v140, v141
	v_cndmask_b32_e64 v160, v157, v154, s[28:29]
	v_exp_f32_e32 v160, v160
	v_add_f32_e32 v152, 1.0, v152
	v_rcp_f32_e32 v159, v152
	v_add_f32_e32 v160, 1.0, v160
	v_rcp_f32_e32 v160, v160
	ds_read_b32 v136, v163 offset:9600
	ds_read_b32 v140, v164 offset:9600
	ds_read_b32 v148, v165 offset:9600
	v_mov_b32_e32 v144, v113
	v_fma_f32 v159, v159, -2.0, 1.0
	ds_read_b32 v152, v166 offset:9600
	v_sub_f32_e32 v153, v161, v159
	v_fma_mixlo_f16 v162, v160, v153, v159
	ds_write_b16 v168, v162 offset:384
	v_fma_f32 v161, v160, v153, v159
	v_mov_b32_e32 v137, 0
	v_mov_b32_e32 v141, 0
	v_mov_b32_e32 v145, 0
	v_mov_b32_e32 v149, 0
	global_store_dword v[170:171], v161, off
	v_lshl_add_u64 v[170:171], v[170:171], 0, s[20:21]
	s_waitcnt lgkmcnt(0)
	s_barrier
	ds_read_b128 v[116:119], v167 offset:384
	ds_read_b128 v[120:123], v167 offset:512
	ds_read_b128 v[124:127], v167 offset:640
	s_waitcnt lgkmcnt(2)
	v_smfmac_f32_16x16x64_f16 v[136:139], v[116:119], v[16:23], v112
	v_smfmac_f32_16x16x64_f16 v[148:151], v[116:119], v[88:95], v112
	s_waitcnt lgkmcnt(1)
	v_smfmac_f32_16x16x64_f16 v[136:139], v[120:123], v[24:31], v112
	v_smfmac_f32_16x16x64_f16 v[148:151], v[120:123], v[96:103], v112
	s_waitcnt lgkmcnt(0)
	v_smfmac_f32_16x16x64_f16 v[136:139], v[124:127], v[32:39], v112
	v_smfmac_f32_16x16x64_f16 v[148:151], v[124:127], v[104:111], v112
	v_smfmac_f32_16x16x64_f16 v[144:147], v[116:119], v[64:71], v112
	v_smfmac_f32_16x16x64_f16 v[140:143], v[116:119], v[40:47], v112
	v_smfmac_f32_16x16x64_f16 v[144:147], v[120:123], v[72:79], v112
	v_smfmac_f32_16x16x64_f16 v[140:143], v[120:123], v[48:55], v112
	s_nop 3
	v_add_f32_e32 v153, v136, v137
	v_add_f32_e32 v156, v148, v149
	v_smfmac_f32_16x16x64_f16 v[144:147], v[124:127], v[80:87], v112
	v_cndmask_b32_e64 v159, v156, v153, s[28:29]
	v_exp_f32_e32 v159, v159
	v_smfmac_f32_16x16x64_f16 v[140:143], v[124:127], v[56:63], v112
	v_mov_b32_dpp v157, v156 row_shl:3 row_mask:0xf bank_mask:0xf bound_ctrl:1
	v_mov_b32_dpp v158, v156 row_shl:6 row_mask:0xf bank_mask:0xf bound_ctrl:1
	v_add_f32_e32 v159, 1.0, v159
	v_rcp_f32_e32 v159, v159
	s_nop 0
	v_add_f32_e32 v155, v144, v145
	v_cndmask_b32_e64 v155, v158, v155, s[28:29]
	v_fmac_f32_e32 v152, v159, v155
	v_exp_f32_e32 v152, v152
	v_add_f32_e32 v154, v140, v141
	v_cndmask_b32_e64 v160, v157, v154, s[28:29]
	v_exp_f32_e32 v160, v160
	v_add_f32_e32 v152, 1.0, v152
	v_rcp_f32_e32 v159, v152
	v_add_f32_e32 v160, 1.0, v160
	v_rcp_f32_e32 v160, v160
	ds_read_b32 v136, v163 offset:11520
	ds_read_b32 v140, v164 offset:11520
	ds_read_b32 v148, v165 offset:11520
	v_mov_b32_e32 v144, v113
	v_fma_f32 v159, v159, -2.0, 1.0
	ds_read_b32 v152, v166 offset:11520
	v_sub_f32_e32 v153, v161, v159
	v_fma_mixlo_f16 v162, v160, v153, v159
	ds_write_b16 v168, v162 offset:0
	v_fma_f32 v161, v160, v153, v159
	v_mov_b32_e32 v137, 0
	v_mov_b32_e32 v141, 0
	v_mov_b32_e32 v145, 0
	v_mov_b32_e32 v149, 0
	global_store_dword v[170:171], v161, off
	v_lshl_add_u64 v[170:171], v[170:171], 0, s[20:21]
	s_waitcnt lgkmcnt(0)
	s_barrier
	ds_read_b128 v[116:119], v167 offset:0
	ds_read_b128 v[120:123], v167 offset:128
	ds_read_b128 v[124:127], v167 offset:256
	s_waitcnt lgkmcnt(2)
	v_smfmac_f32_16x16x64_f16 v[136:139], v[116:119], v[16:23], v112
	v_smfmac_f32_16x16x64_f16 v[148:151], v[116:119], v[88:95], v112
	s_waitcnt lgkmcnt(1)
	v_smfmac_f32_16x16x64_f16 v[136:139], v[120:123], v[24:31], v112
	v_smfmac_f32_16x16x64_f16 v[148:151], v[120:123], v[96:103], v112
	s_waitcnt lgkmcnt(0)
	v_smfmac_f32_16x16x64_f16 v[136:139], v[124:127], v[32:39], v112
	v_smfmac_f32_16x16x64_f16 v[148:151], v[124:127], v[104:111], v112
	v_smfmac_f32_16x16x64_f16 v[144:147], v[116:119], v[64:71], v112
	v_smfmac_f32_16x16x64_f16 v[140:143], v[116:119], v[40:47], v112
	v_smfmac_f32_16x16x64_f16 v[144:147], v[120:123], v[72:79], v112
	v_smfmac_f32_16x16x64_f16 v[140:143], v[120:123], v[48:55], v112
	s_nop 3
	v_add_f32_e32 v153, v136, v137
	v_add_f32_e32 v156, v148, v149
	v_smfmac_f32_16x16x64_f16 v[144:147], v[124:127], v[80:87], v112
	v_cndmask_b32_e64 v159, v156, v153, s[28:29]
	v_exp_f32_e32 v159, v159
	v_smfmac_f32_16x16x64_f16 v[140:143], v[124:127], v[56:63], v112
	v_mov_b32_dpp v157, v156 row_shl:3 row_mask:0xf bank_mask:0xf bound_ctrl:1
	v_mov_b32_dpp v158, v156 row_shl:6 row_mask:0xf bank_mask:0xf bound_ctrl:1
	v_add_f32_e32 v159, 1.0, v159
	v_rcp_f32_e32 v159, v159
	s_nop 0
	v_add_f32_e32 v155, v144, v145
	v_cndmask_b32_e64 v155, v158, v155, s[28:29]
	v_fmac_f32_e32 v152, v159, v155
	v_exp_f32_e32 v152, v152
	v_add_f32_e32 v154, v140, v141
	v_cndmask_b32_e64 v160, v157, v154, s[28:29]
	v_exp_f32_e32 v160, v160
	v_add_f32_e32 v152, 1.0, v152
	v_rcp_f32_e32 v159, v152
	v_add_f32_e32 v160, 1.0, v160
	v_rcp_f32_e32 v160, v160
	ds_read_b32 v136, v163 offset:13440
	ds_read_b32 v140, v164 offset:13440
	ds_read_b32 v148, v165 offset:13440
	v_mov_b32_e32 v144, v113
	v_fma_f32 v159, v159, -2.0, 1.0
	ds_read_b32 v152, v166 offset:13440
	v_sub_f32_e32 v153, v161, v159
	v_fma_mixlo_f16 v162, v160, v153, v159
	ds_write_b16 v168, v162 offset:384
	v_fma_f32 v161, v160, v153, v159
	v_mov_b32_e32 v137, 0
	v_mov_b32_e32 v141, 0
	v_mov_b32_e32 v145, 0
	v_mov_b32_e32 v149, 0
	global_store_dword v[170:171], v161, off
	v_lshl_add_u64 v[170:171], v[170:171], 0, s[20:21]
	s_waitcnt lgkmcnt(0)
	s_barrier
	ds_read_b128 v[116:119], v167 offset:384
	ds_read_b128 v[120:123], v167 offset:512
	ds_read_b128 v[124:127], v167 offset:640
	s_waitcnt lgkmcnt(2)
	v_smfmac_f32_16x16x64_f16 v[136:139], v[116:119], v[16:23], v112
	v_smfmac_f32_16x16x64_f16 v[148:151], v[116:119], v[88:95], v112
	s_waitcnt lgkmcnt(1)
	v_smfmac_f32_16x16x64_f16 v[136:139], v[120:123], v[24:31], v112
	v_smfmac_f32_16x16x64_f16 v[148:151], v[120:123], v[96:103], v112
	s_waitcnt lgkmcnt(0)
	v_smfmac_f32_16x16x64_f16 v[136:139], v[124:127], v[32:39], v112
	v_smfmac_f32_16x16x64_f16 v[148:151], v[124:127], v[104:111], v112
	v_smfmac_f32_16x16x64_f16 v[144:147], v[116:119], v[64:71], v112
	v_smfmac_f32_16x16x64_f16 v[140:143], v[116:119], v[40:47], v112
	v_smfmac_f32_16x16x64_f16 v[144:147], v[120:123], v[72:79], v112
	v_smfmac_f32_16x16x64_f16 v[140:143], v[120:123], v[48:55], v112
	s_nop 3
	v_add_f32_e32 v153, v136, v137
	v_add_f32_e32 v156, v148, v149
	v_smfmac_f32_16x16x64_f16 v[144:147], v[124:127], v[80:87], v112
	v_cndmask_b32_e64 v159, v156, v153, s[28:29]
	v_exp_f32_e32 v159, v159
	v_smfmac_f32_16x16x64_f16 v[140:143], v[124:127], v[56:63], v112
	v_mov_b32_dpp v157, v156 row_shl:3 row_mask:0xf bank_mask:0xf bound_ctrl:1
	v_mov_b32_dpp v158, v156 row_shl:6 row_mask:0xf bank_mask:0xf bound_ctrl:1
	v_add_f32_e32 v159, 1.0, v159
	v_rcp_f32_e32 v159, v159
	s_nop 0
	v_add_f32_e32 v155, v144, v145
	v_cndmask_b32_e64 v155, v158, v155, s[28:29]
	v_fmac_f32_e32 v152, v159, v155
	v_exp_f32_e32 v152, v152
	v_add_f32_e32 v154, v140, v141
	v_cndmask_b32_e64 v160, v157, v154, s[28:29]
	v_exp_f32_e32 v160, v160
	v_add_f32_e32 v152, 1.0, v152
	v_rcp_f32_e32 v159, v152
	v_add_f32_e32 v160, 1.0, v160
	v_rcp_f32_e32 v160, v160
	ds_read_b32 v136, v163 offset:15360
	ds_read_b32 v140, v164 offset:15360
	ds_read_b32 v148, v165 offset:15360
	v_mov_b32_e32 v144, v113
	v_fma_f32 v159, v159, -2.0, 1.0
	ds_read_b32 v152, v166 offset:15360
	v_sub_f32_e32 v153, v161, v159
	v_fma_mixlo_f16 v162, v160, v153, v159
	ds_write_b16 v168, v162 offset:0
	v_fma_f32 v161, v160, v153, v159
	v_mov_b32_e32 v137, 0
	v_mov_b32_e32 v141, 0
	v_mov_b32_e32 v145, 0
	v_mov_b32_e32 v149, 0
	global_store_dword v[170:171], v161, off
	v_lshl_add_u64 v[170:171], v[170:171], 0, s[20:21]
	s_waitcnt lgkmcnt(0)
	s_barrier
	ds_read_b128 v[116:119], v167 offset:0
	ds_read_b128 v[120:123], v167 offset:128
	ds_read_b128 v[124:127], v167 offset:256
	s_waitcnt lgkmcnt(2)
	v_smfmac_f32_16x16x64_f16 v[136:139], v[116:119], v[16:23], v112
	v_smfmac_f32_16x16x64_f16 v[148:151], v[116:119], v[88:95], v112
	s_waitcnt lgkmcnt(1)
	v_smfmac_f32_16x16x64_f16 v[136:139], v[120:123], v[24:31], v112
	v_smfmac_f32_16x16x64_f16 v[148:151], v[120:123], v[96:103], v112
	s_waitcnt lgkmcnt(0)
	v_smfmac_f32_16x16x64_f16 v[136:139], v[124:127], v[32:39], v112
	v_smfmac_f32_16x16x64_f16 v[148:151], v[124:127], v[104:111], v112
	v_smfmac_f32_16x16x64_f16 v[144:147], v[116:119], v[64:71], v112
	v_smfmac_f32_16x16x64_f16 v[140:143], v[116:119], v[40:47], v112
	v_smfmac_f32_16x16x64_f16 v[144:147], v[120:123], v[72:79], v112
	v_smfmac_f32_16x16x64_f16 v[140:143], v[120:123], v[48:55], v112
	s_nop 3
	v_add_f32_e32 v153, v136, v137
	v_add_f32_e32 v156, v148, v149
	v_smfmac_f32_16x16x64_f16 v[144:147], v[124:127], v[80:87], v112
	v_cndmask_b32_e64 v159, v156, v153, s[28:29]
	v_exp_f32_e32 v159, v159
	v_smfmac_f32_16x16x64_f16 v[140:143], v[124:127], v[56:63], v112
	v_mov_b32_dpp v157, v156 row_shl:3 row_mask:0xf bank_mask:0xf bound_ctrl:1
	v_mov_b32_dpp v158, v156 row_shl:6 row_mask:0xf bank_mask:0xf bound_ctrl:1
	v_add_f32_e32 v159, 1.0, v159
	v_rcp_f32_e32 v159, v159
	s_nop 0
	v_add_f32_e32 v155, v144, v145
	v_cndmask_b32_e64 v155, v158, v155, s[28:29]
	v_fmac_f32_e32 v152, v159, v155
	v_exp_f32_e32 v152, v152
	v_add_f32_e32 v154, v140, v141
	v_cndmask_b32_e64 v160, v157, v154, s[28:29]
	v_exp_f32_e32 v160, v160
	v_add_f32_e32 v152, 1.0, v152
	v_rcp_f32_e32 v159, v152
	v_add_f32_e32 v160, 1.0, v160
	v_rcp_f32_e32 v160, v160
	ds_read_b32 v136, v163 offset:17280
	ds_read_b32 v140, v164 offset:17280
	ds_read_b32 v148, v165 offset:17280
	v_mov_b32_e32 v144, v113
	v_fma_f32 v159, v159, -2.0, 1.0
	ds_read_b32 v152, v166 offset:17280
	v_sub_f32_e32 v153, v161, v159
	v_fma_mixlo_f16 v162, v160, v153, v159
	ds_write_b16 v168, v162 offset:384
	v_fma_f32 v161, v160, v153, v159
	v_mov_b32_e32 v137, 0
	v_mov_b32_e32 v141, 0
	v_mov_b32_e32 v145, 0
	v_mov_b32_e32 v149, 0
	global_store_dword v[170:171], v161, off
	v_lshl_add_u64 v[170:171], v[170:171], 0, s[20:21]
	s_waitcnt lgkmcnt(0)
	s_barrier
	ds_read_b128 v[116:119], v167 offset:384
	ds_read_b128 v[120:123], v167 offset:512
	ds_read_b128 v[124:127], v167 offset:640
	s_waitcnt lgkmcnt(2)
	v_smfmac_f32_16x16x64_f16 v[136:139], v[116:119], v[16:23], v112
	v_smfmac_f32_16x16x64_f16 v[148:151], v[116:119], v[88:95], v112
	s_waitcnt lgkmcnt(1)
	v_smfmac_f32_16x16x64_f16 v[136:139], v[120:123], v[24:31], v112
	v_smfmac_f32_16x16x64_f16 v[148:151], v[120:123], v[96:103], v112
	s_waitcnt lgkmcnt(0)
	v_smfmac_f32_16x16x64_f16 v[136:139], v[124:127], v[32:39], v112
	v_smfmac_f32_16x16x64_f16 v[148:151], v[124:127], v[104:111], v112
	s_cmp_eq_u32 s26, 7
	s_cbranch_scc1 .Lgru1_nost0
	s_waitcnt vmcnt(4)
	v_mul_f32_e32 v176, s51, v176
	v_mul_f32_e32 v177, s51, v177
	v_mul_f32_e32 v178, s51, v178
	v_mul_f32_e32 v179, s51, v179
	v_mul_f32_e32 v180, v175, v180
	v_mul_f32_e32 v181, v175, v181
	v_mul_f32_e32 v182, s52, v182
	v_mul_f32_e32 v183, s52, v183
	ds_write_b64 v173, v[176:177] offset:0
	ds_write_b64 v173, v[178:179] offset:512
	ds_write_b64 v173, v[180:181] offset:1024
	ds_write_b64 v115, v[182:183] offset:1536
.Lgru1_nost0:
	v_smfmac_f32_16x16x64_f16 v[144:147], v[116:119], v[64:71], v112
	v_smfmac_f32_16x16x64_f16 v[140:143], v[116:119], v[40:47], v112
	v_smfmac_f32_16x16x64_f16 v[144:147], v[120:123], v[72:79], v112
	v_smfmac_f32_16x16x64_f16 v[140:143], v[120:123], v[48:55], v112
	s_nop 3
	v_add_f32_e32 v153, v136, v137
	v_add_f32_e32 v156, v148, v149
	v_smfmac_f32_16x16x64_f16 v[144:147], v[124:127], v[80:87], v112
	v_cndmask_b32_e64 v159, v156, v153, s[28:29]
	v_exp_f32_e32 v159, v159
	v_smfmac_f32_16x16x64_f16 v[140:143], v[124:127], v[56:63], v112
	v_mov_b32_dpp v157, v156 row_shl:3 row_mask:0xf bank_mask:0xf bound_ctrl:1
	v_mov_b32_dpp v158, v156 row_shl:6 row_mask:0xf bank_mask:0xf bound_ctrl:1
	v_add_f32_e32 v159, 1.0, v159
	v_rcp_f32_e32 v159, v159
	s_nop 0
	v_add_f32_e32 v155, v144, v145
	v_cndmask_b32_e64 v155, v158, v155, s[28:29]
	v_fmac_f32_e32 v152, v159, v155
	v_exp_f32_e32 v152, v152
	v_add_f32_e32 v154, v140, v141
	v_cndmask_b32_e64 v160, v157, v154, s[28:29]
	v_exp_f32_e32 v160, v160
	v_add_f32_e32 v152, 1.0, v152
	v_rcp_f32_e32 v159, v152
	v_add_f32_e32 v160, 1.0, v160
	v_rcp_f32_e32 v160, v160
	ds_read_b32 v136, v163 offset:19200
	ds_read_b32 v140, v164 offset:19200
	ds_read_b32 v148, v165 offset:19200
	v_mov_b32_e32 v144, v113
	v_fma_f32 v159, v159, -2.0, 1.0
	ds_read_b32 v152, v166 offset:19200
	v_sub_f32_e32 v153, v161, v159
	v_fma_mixlo_f16 v162, v160, v153, v159
	ds_write_b16 v168, v162 offset:0
	v_fma_f32 v161, v160, v153, v159
	v_mov_b32_e32 v137, 0
	v_mov_b32_e32 v141, 0
	v_mov_b32_e32 v145, 0
	v_mov_b32_e32 v149, 0
	global_store_dword v[170:171], v161, off
	v_lshl_add_u64 v[170:171], v[170:171], 0, s[20:21]
	s_waitcnt lgkmcnt(0)
	s_barrier
	ds_read_b128 v[116:119], v167 offset:0
	ds_read_b128 v[120:123], v167 offset:128
	ds_read_b128 v[124:127], v167 offset:256
	s_waitcnt lgkmcnt(2)
	v_smfmac_f32_16x16x64_f16 v[136:139], v[116:119], v[16:23], v112
	v_smfmac_f32_16x16x64_f16 v[148:151], v[116:119], v[88:95], v112
	s_waitcnt lgkmcnt(1)
	v_smfmac_f32_16x16x64_f16 v[136:139], v[120:123], v[24:31], v112
	v_smfmac_f32_16x16x64_f16 v[148:151], v[120:123], v[96:103], v112
	s_waitcnt lgkmcnt(0)
	v_smfmac_f32_16x16x64_f16 v[136:139], v[124:127], v[32:39], v112
	v_smfmac_f32_16x16x64_f16 v[148:151], v[124:127], v[104:111], v112
	v_smfmac_f32_16x16x64_f16 v[144:147], v[116:119], v[64:71], v112
	v_smfmac_f32_16x16x64_f16 v[140:143], v[116:119], v[40:47], v112
	v_smfmac_f32_16x16x64_f16 v[144:147], v[120:123], v[72:79], v112
	v_smfmac_f32_16x16x64_f16 v[140:143], v[120:123], v[48:55], v112
	s_nop 3
	v_add_f32_e32 v153, v136, v137
	v_add_f32_e32 v156, v148, v149
	v_smfmac_f32_16x16x64_f16 v[144:147], v[124:127], v[80:87], v112
	v_cndmask_b32_e64 v159, v156, v153, s[28:29]
	v_exp_f32_e32 v159, v159
	v_smfmac_f32_16x16x64_f16 v[140:143], v[124:127], v[56:63], v112
	v_mov_b32_dpp v157, v156 row_shl:3 row_mask:0xf bank_mask:0xf bound_ctrl:1
	v_mov_b32_dpp v158, v156 row_shl:6 row_mask:0xf bank_mask:0xf bound_ctrl:1
	v_add_f32_e32 v159, 1.0, v159
	v_rcp_f32_e32 v159, v159
	s_nop 0
	v_add_f32_e32 v155, v144, v145
	v_cndmask_b32_e64 v155, v158, v155, s[28:29]
	v_fmac_f32_e32 v152, v159, v155
	v_exp_f32_e32 v152, v152
	v_add_f32_e32 v154, v140, v141
	v_cndmask_b32_e64 v160, v157, v154, s[28:29]
	v_exp_f32_e32 v160, v160
	v_add_f32_e32 v152, 1.0, v152
	v_rcp_f32_e32 v159, v152
	v_add_f32_e32 v160, 1.0, v160
	v_rcp_f32_e32 v160, v160
	ds_read_b32 v136, v163 offset:21120
	ds_read_b32 v140, v164 offset:21120
	ds_read_b32 v148, v165 offset:21120
	v_mov_b32_e32 v144, v113
	v_fma_f32 v159, v159, -2.0, 1.0
	ds_read_b32 v152, v166 offset:21120
	v_sub_f32_e32 v153, v161, v159
	v_fma_mixlo_f16 v162, v160, v153, v159
	ds_write_b16 v168, v162 offset:384
	v_fma_f32 v161, v160, v153, v159
	v_mov_b32_e32 v137, 0
	v_mov_b32_e32 v141, 0
	v_mov_b32_e32 v145, 0
	v_mov_b32_e32 v149, 0
	global_store_dword v[170:171], v161, off
	v_lshl_add_u64 v[170:171], v[170:171], 0, s[20:21]
	s_waitcnt lgkmcnt(0)
	s_barrier
	ds_read_b128 v[116:119], v167 offset:384
	ds_read_b128 v[120:123], v167 offset:512
	ds_read_b128 v[124:127], v167 offset:640
	s_waitcnt lgkmcnt(2)
	v_smfmac_f32_16x16x64_f16 v[136:139], v[116:119], v[16:23], v112
	v_smfmac_f32_16x16x64_f16 v[148:151], v[116:119], v[88:95], v112
	s_waitcnt lgkmcnt(1)
	v_smfmac_f32_16x16x64_f16 v[136:139], v[120:123], v[24:31], v112
	v_smfmac_f32_16x16x64_f16 v[148:151], v[120:123], v[96:103], v112
	s_waitcnt lgkmcnt(0)
	v_smfmac_f32_16x16x64_f16 v[136:139], v[124:127], v[32:39], v112
	v_smfmac_f32_16x16x64_f16 v[148:151], v[124:127], v[104:111], v112
	s_cmp_eq_u32 s26, 7
	s_cbranch_scc1 .Lgru1_nost1
	s_waitcnt vmcnt(4)
	v_mul_f32_e32 v184, s51, v184
	v_mul_f32_e32 v185, s51, v185
	v_mul_f32_e32 v186, s51, v186
	v_mul_f32_e32 v187, s51, v187
	v_mul_f32_e32 v188, v175, v188
	v_mul_f32_e32 v189, v175, v189
	v_mul_f32_e32 v190, s52, v190
	v_mul_f32_e32 v191, s52, v191
	ds_write_b64 v174, v[184:185] offset:0
	ds_write_b64 v174, v[186:187] offset:512
	ds_write_b64 v174, v[188:189] offset:1024
	ds_write_b64 v169, v[190:191] offset:1536
.Lgru1_nost1:
	v_smfmac_f32_16x16x64_f16 v[144:147], v[116:119], v[64:71], v112
	v_smfmac_f32_16x16x64_f16 v[140:143], v[116:119], v[40:47], v112
	v_smfmac_f32_16x16x64_f16 v[144:147], v[120:123], v[72:79], v112
	v_smfmac_f32_16x16x64_f16 v[140:143], v[120:123], v[48:55], v112
	s_nop 3
	v_add_f32_e32 v153, v136, v137
	v_add_f32_e32 v156, v148, v149
	v_smfmac_f32_16x16x64_f16 v[144:147], v[124:127], v[80:87], v112
	v_cndmask_b32_e64 v159, v156, v153, s[28:29]
	v_exp_f32_e32 v159, v159
	v_smfmac_f32_16x16x64_f16 v[140:143], v[124:127], v[56:63], v112
	v_mov_b32_dpp v157, v156 row_shl:3 row_mask:0xf bank_mask:0xf bound_ctrl:1
	v_mov_b32_dpp v158, v156 row_shl:6 row_mask:0xf bank_mask:0xf bound_ctrl:1
	v_add_f32_e32 v159, 1.0, v159
	v_rcp_f32_e32 v159, v159
	s_nop 0
	v_add_f32_e32 v155, v144, v145
	v_cndmask_b32_e64 v155, v158, v155, s[28:29]
	v_fmac_f32_e32 v152, v159, v155
	v_exp_f32_e32 v152, v152
	v_add_f32_e32 v154, v140, v141
	v_cndmask_b32_e64 v160, v157, v154, s[28:29]
	v_exp_f32_e32 v160, v160
	v_add_f32_e32 v152, 1.0, v152
	v_rcp_f32_e32 v159, v152
	v_add_f32_e32 v160, 1.0, v160
	v_rcp_f32_e32 v160, v160
	ds_read_b32 v136, v163 offset:23040
	ds_read_b32 v140, v164 offset:23040
	ds_read_b32 v148, v165 offset:23040
	v_mov_b32_e32 v144, v113
	v_fma_f32 v159, v159, -2.0, 1.0
	ds_read_b32 v152, v166 offset:23040
	v_sub_f32_e32 v153, v161, v159
	v_fma_mixlo_f16 v162, v160, v153, v159
	ds_write_b16 v168, v162 offset:0
	v_fma_f32 v161, v160, v153, v159
	v_mov_b32_e32 v137, 0
	v_mov_b32_e32 v141, 0
	v_mov_b32_e32 v145, 0
	v_mov_b32_e32 v149, 0
	global_store_dword v[170:171], v161, off
	v_lshl_add_u64 v[170:171], v[170:171], 0, s[20:21]
	s_waitcnt lgkmcnt(0)
	s_barrier
	ds_read_b128 v[116:119], v167 offset:0
	ds_read_b128 v[120:123], v167 offset:128
	ds_read_b128 v[124:127], v167 offset:256
	s_waitcnt lgkmcnt(2)
	v_smfmac_f32_16x16x64_f16 v[136:139], v[116:119], v[16:23], v112
	v_smfmac_f32_16x16x64_f16 v[148:151], v[116:119], v[88:95], v112
	s_waitcnt lgkmcnt(1)
	v_smfmac_f32_16x16x64_f16 v[136:139], v[120:123], v[24:31], v112
	v_smfmac_f32_16x16x64_f16 v[148:151], v[120:123], v[96:103], v112
	s_waitcnt lgkmcnt(0)
	v_smfmac_f32_16x16x64_f16 v[136:139], v[124:127], v[32:39], v112
	v_smfmac_f32_16x16x64_f16 v[148:151], v[124:127], v[104:111], v112
	v_smfmac_f32_16x16x64_f16 v[144:147], v[116:119], v[64:71], v112
	v_smfmac_f32_16x16x64_f16 v[140:143], v[116:119], v[40:47], v112
	v_smfmac_f32_16x16x64_f16 v[144:147], v[120:123], v[72:79], v112
	v_smfmac_f32_16x16x64_f16 v[140:143], v[120:123], v[48:55], v112
	s_nop 3
	v_add_f32_e32 v153, v136, v137
	v_add_f32_e32 v156, v148, v149
	v_smfmac_f32_16x16x64_f16 v[144:147], v[124:127], v[80:87], v112
	v_cndmask_b32_e64 v159, v156, v153, s[28:29]
	v_exp_f32_e32 v159, v159
	v_smfmac_f32_16x16x64_f16 v[140:143], v[124:127], v[56:63], v112
	v_mov_b32_dpp v157, v156 row_shl:3 row_mask:0xf bank_mask:0xf bound_ctrl:1
	v_mov_b32_dpp v158, v156 row_shl:6 row_mask:0xf bank_mask:0xf bound_ctrl:1
	v_add_f32_e32 v159, 1.0, v159
	v_rcp_f32_e32 v159, v159
	s_nop 0
	v_add_f32_e32 v155, v144, v145
	v_cndmask_b32_e64 v155, v158, v155, s[28:29]
	v_fmac_f32_e32 v152, v159, v155
	v_exp_f32_e32 v152, v152
	v_add_f32_e32 v154, v140, v141
	v_cndmask_b32_e64 v160, v157, v154, s[28:29]
	v_exp_f32_e32 v160, v160
	v_add_f32_e32 v152, 1.0, v152
	v_rcp_f32_e32 v159, v152
	v_add_f32_e32 v160, 1.0, v160
	v_rcp_f32_e32 v160, v160
	ds_read_b32 v136, v163 offset:24960
	ds_read_b32 v140, v164 offset:24960
	ds_read_b32 v148, v165 offset:24960
	v_mov_b32_e32 v144, v113
	v_fma_f32 v159, v159, -2.0, 1.0
	ds_read_b32 v152, v166 offset:24960
	v_sub_f32_e32 v153, v161, v159
	v_fma_mixlo_f16 v162, v160, v153, v159
	ds_write_b16 v168, v162 offset:384
	v_fma_f32 v161, v160, v153, v159
	v_mov_b32_e32 v137, 0
	v_mov_b32_e32 v141, 0
	v_mov_b32_e32 v145, 0
	v_mov_b32_e32 v149, 0
	global_store_dword v[170:171], v161, off
	v_lshl_add_u64 v[170:171], v[170:171], 0, s[20:21]
	s_waitcnt lgkmcnt(0)
	s_barrier
	ds_read_b128 v[116:119], v167 offset:384
	ds_read_b128 v[120:123], v167 offset:512
	ds_read_b128 v[124:127], v167 offset:640
	s_waitcnt lgkmcnt(2)
	v_smfmac_f32_16x16x64_f16 v[136:139], v[116:119], v[16:23], v112
	v_smfmac_f32_16x16x64_f16 v[148:151], v[116:119], v[88:95], v112
	s_waitcnt lgkmcnt(1)
	v_smfmac_f32_16x16x64_f16 v[136:139], v[120:123], v[24:31], v112
	v_smfmac_f32_16x16x64_f16 v[148:151], v[120:123], v[96:103], v112
	s_waitcnt lgkmcnt(0)
	v_smfmac_f32_16x16x64_f16 v[136:139], v[124:127], v[32:39], v112
	v_smfmac_f32_16x16x64_f16 v[148:151], v[124:127], v[104:111], v112
	v_smfmac_f32_16x16x64_f16 v[144:147], v[116:119], v[64:71], v112
	v_smfmac_f32_16x16x64_f16 v[140:143], v[116:119], v[40:47], v112
	v_smfmac_f32_16x16x64_f16 v[144:147], v[120:123], v[72:79], v112
	v_smfmac_f32_16x16x64_f16 v[140:143], v[120:123], v[48:55], v112
	s_nop 3
	v_add_f32_e32 v153, v136, v137
	v_add_f32_e32 v156, v148, v149
	v_smfmac_f32_16x16x64_f16 v[144:147], v[124:127], v[80:87], v112
	v_cndmask_b32_e64 v159, v156, v153, s[28:29]
	v_exp_f32_e32 v159, v159
	v_smfmac_f32_16x16x64_f16 v[140:143], v[124:127], v[56:63], v112
	v_mov_b32_dpp v157, v156 row_shl:3 row_mask:0xf bank_mask:0xf bound_ctrl:1
	v_mov_b32_dpp v158, v156 row_shl:6 row_mask:0xf bank_mask:0xf bound_ctrl:1
	v_add_f32_e32 v159, 1.0, v159
	v_rcp_f32_e32 v159, v159
	s_nop 0
	v_add_f32_e32 v155, v144, v145
	v_cndmask_b32_e64 v155, v158, v155, s[28:29]
	v_fmac_f32_e32 v152, v159, v155
	v_exp_f32_e32 v152, v152
	v_add_f32_e32 v154, v140, v141
	v_cndmask_b32_e64 v160, v157, v154, s[28:29]
	v_exp_f32_e32 v160, v160
	v_add_f32_e32 v152, 1.0, v152
	v_rcp_f32_e32 v159, v152
	v_add_f32_e32 v160, 1.0, v160
	v_rcp_f32_e32 v160, v160
	ds_read_b32 v136, v163 offset:26880
	ds_read_b32 v140, v164 offset:26880
	ds_read_b32 v148, v165 offset:26880
	v_mov_b32_e32 v144, v113
	v_fma_f32 v159, v159, -2.0, 1.0
	ds_read_b32 v152, v166 offset:26880
	v_sub_f32_e32 v153, v161, v159
	v_fma_mixlo_f16 v162, v160, v153, v159
	ds_write_b16 v168, v162 offset:0
	v_fma_f32 v161, v160, v153, v159
	v_mov_b32_e32 v137, 0
	v_mov_b32_e32 v141, 0
	v_mov_b32_e32 v145, 0
	v_mov_b32_e32 v149, 0
	global_store_dword v[170:171], v161, off
	v_lshl_add_u64 v[170:171], v[170:171], 0, s[20:21]
	s_waitcnt lgkmcnt(0)
	s_barrier
	ds_read_b128 v[116:119], v167 offset:0
	ds_read_b128 v[120:123], v167 offset:128
	ds_read_b128 v[124:127], v167 offset:256
	s_waitcnt lgkmcnt(2)
	v_smfmac_f32_16x16x64_f16 v[136:139], v[116:119], v[16:23], v112
	v_smfmac_f32_16x16x64_f16 v[148:151], v[116:119], v[88:95], v112
	s_waitcnt lgkmcnt(1)
	v_smfmac_f32_16x16x64_f16 v[136:139], v[120:123], v[24:31], v112
	v_smfmac_f32_16x16x64_f16 v[148:151], v[120:123], v[96:103], v112
	s_waitcnt lgkmcnt(0)
	v_smfmac_f32_16x16x64_f16 v[136:139], v[124:127], v[32:39], v112
	v_smfmac_f32_16x16x64_f16 v[148:151], v[124:127], v[104:111], v112
	v_smfmac_f32_16x16x64_f16 v[144:147], v[116:119], v[64:71], v112
	v_smfmac_f32_16x16x64_f16 v[140:143], v[116:119], v[40:47], v112
	v_smfmac_f32_16x16x64_f16 v[144:147], v[120:123], v[72:79], v112
	v_smfmac_f32_16x16x64_f16 v[140:143], v[120:123], v[48:55], v112
	s_nop 3
	v_add_f32_e32 v153, v136, v137
	v_add_f32_e32 v156, v148, v149
	v_smfmac_f32_16x16x64_f16 v[144:147], v[124:127], v[80:87], v112
	v_cndmask_b32_e64 v159, v156, v153, s[28:29]
	v_exp_f32_e32 v159, v159
	v_smfmac_f32_16x16x64_f16 v[140:143], v[124:127], v[56:63], v112
	v_mov_b32_dpp v157, v156 row_shl:3 row_mask:0xf bank_mask:0xf bound_ctrl:1
	v_mov_b32_dpp v158, v156 row_shl:6 row_mask:0xf bank_mask:0xf bound_ctrl:1
	v_add_f32_e32 v159, 1.0, v159
	v_rcp_f32_e32 v159, v159
	s_nop 0
	v_add_f32_e32 v155, v144, v145
	v_cndmask_b32_e64 v155, v158, v155, s[28:29]
	v_fmac_f32_e32 v152, v159, v155
	v_exp_f32_e32 v152, v152
	v_add_f32_e32 v154, v140, v141
	v_cndmask_b32_e64 v160, v157, v154, s[28:29]
	v_exp_f32_e32 v160, v160
	v_add_f32_e32 v152, 1.0, v152
	v_rcp_f32_e32 v159, v152
	v_add_f32_e32 v160, 1.0, v160
	v_rcp_f32_e32 v160, v160
	ds_read_b32 v136, v163 offset:28800
	ds_read_b32 v140, v164 offset:28800
	ds_read_b32 v148, v165 offset:28800
	v_mov_b32_e32 v144, v113
	v_fma_f32 v159, v159, -2.0, 1.0
	ds_read_b32 v152, v166 offset:28800
	v_sub_f32_e32 v153, v161, v159
	v_fma_mixlo_f16 v162, v160, v153, v159
	ds_write_b16 v168, v162 offset:384
	v_fma_f32 v161, v160, v153, v159
	v_mov_b32_e32 v137, 0
	v_mov_b32_e32 v141, 0
	v_mov_b32_e32 v145, 0
	v_mov_b32_e32 v149, 0
	global_store_dword v[170:171], v161, off
	v_lshl_add_u64 v[170:171], v[170:171], 0, s[20:21]
	s_waitcnt lgkmcnt(0)
	s_barrier
	ds_read_b128 v[116:119], v167 offset:384
	ds_read_b128 v[120:123], v167 offset:512
	ds_read_b128 v[124:127], v167 offset:640
	s_waitcnt lgkmcnt(2)
	v_smfmac_f32_16x16x64_f16 v[136:139], v[116:119], v[16:23], v112
	v_smfmac_f32_16x16x64_f16 v[148:151], v[116:119], v[88:95], v112
	s_waitcnt lgkmcnt(1)
	v_smfmac_f32_16x16x64_f16 v[136:139], v[120:123], v[24:31], v112
	v_smfmac_f32_16x16x64_f16 v[148:151], v[120:123], v[96:103], v112
	s_waitcnt lgkmcnt(0)
	v_smfmac_f32_16x16x64_f16 v[136:139], v[124:127], v[32:39], v112
	v_smfmac_f32_16x16x64_f16 v[148:151], v[124:127], v[104:111], v112
	v_smfmac_f32_16x16x64_f16 v[144:147], v[116:119], v[64:71], v112
	v_smfmac_f32_16x16x64_f16 v[140:143], v[116:119], v[40:47], v112
	v_smfmac_f32_16x16x64_f16 v[144:147], v[120:123], v[72:79], v112
	v_smfmac_f32_16x16x64_f16 v[140:143], v[120:123], v[48:55], v112
	s_nop 3
	v_add_f32_e32 v153, v136, v137
	v_add_f32_e32 v156, v148, v149
	v_smfmac_f32_16x16x64_f16 v[144:147], v[124:127], v[80:87], v112
	v_cndmask_b32_e64 v159, v156, v153, s[28:29]
	v_exp_f32_e32 v159, v159
	v_smfmac_f32_16x16x64_f16 v[140:143], v[124:127], v[56:63], v112
	v_mov_b32_dpp v157, v156 row_shl:3 row_mask:0xf bank_mask:0xf bound_ctrl:1
	v_mov_b32_dpp v158, v156 row_shl:6 row_mask:0xf bank_mask:0xf bound_ctrl:1
	v_add_f32_e32 v159, 1.0, v159
	v_rcp_f32_e32 v159, v159
	v_xor_b32_e32 v163, 0x7800, v163
	v_add_f32_e32 v155, v144, v145
	v_cndmask_b32_e64 v155, v158, v155, s[28:29]
	v_fmac_f32_e32 v152, v159, v155
	v_exp_f32_e32 v152, v152
	v_add_f32_e32 v154, v140, v141
	v_cndmask_b32_e64 v160, v157, v154, s[28:29]
	v_exp_f32_e32 v160, v160
	v_add_f32_e32 v152, 1.0, v152
	v_rcp_f32_e32 v159, v152
	v_xor_b32_e32 v164, 0x7800, v164
	v_xor_b32_e32 v165, 0x7800, v165
	v_add_f32_e32 v160, 1.0, v160
	v_rcp_f32_e32 v160, v160
	v_xor_b32_e32 v166, 0x7800, v166
	v_add_u32_e32 v173, s55, v173
	v_add_u32_e32 v174, s55, v174
	v_add_u32_e32 v115, s55, v115
	v_add_u32_e32 v169, s55, v169
	s_sub_i32 s55, 0, s55
	ds_read_b32 v136, v163 offset:0
	ds_read_b32 v140, v164 offset:0
	ds_read_b32 v148, v165 offset:0
	v_mov_b32_e32 v144, v113
	v_fma_f32 v159, v159, -2.0, 1.0
	ds_read_b32 v152, v166 offset:0
	v_sub_f32_e32 v153, v161, v159
	v_fma_mixlo_f16 v162, v160, v153, v159
	ds_write_b16 v168, v162 offset:0
	v_fma_f32 v161, v160, v153, v159
	v_mov_b32_e32 v137, 0
	v_mov_b32_e32 v141, 0
	v_mov_b32_e32 v145, 0
	v_mov_b32_e32 v149, 0
	global_store_dword v[170:171], v161, off
	v_lshl_add_u64 v[170:171], v[170:171], 0, s[20:21]
	s_waitcnt lgkmcnt(0)
	s_barrier
	s_add_i32 s26, s26, 1
	s_cmp_lt_u32 s26, 8
	s_cbranch_scc1 .Lgru1_chunk
.LBB5_143:
	s_endpgm
	s_nop 0
	s_nop 0
	s_nop 0
	s_nop 0
	s_nop 0
	s_nop 0
	s_nop 0
	s_nop 0
	s_nop 0
	s_nop 0
	s_nop 0
	s_nop 0
	s_nop 0
	s_nop 0
	s_nop 0
	s_nop 0
	s_nop 0
	s_nop 0
	s_nop 0
	s_nop 0
	s_nop 0
	s_nop 0
	s_nop 0
	s_nop 0
	s_nop 0
	s_nop 0
	s_nop 0
	s_nop 0
	s_nop 0
	s_nop 0
	s_nop 0
	s_nop 0
	s_nop 0
	s_nop 0
	s_nop 0
	s_nop 0
	s_nop 0
	s_nop 0
	s_nop 0
	s_nop 0
	s_nop 0
	s_nop 0
	s_nop 0
	s_nop 0
	s_nop 0
	s_nop 0
	s_nop 0
	s_nop 0
	s_nop 0
	s_nop 0
	s_nop 0
	s_nop 0
	s_nop 0
	s_nop 0
	s_nop 0
	s_nop 0
	s_nop 0
	s_nop 0
	s_nop 0
	s_endpgm

.LBB6_26:
	s_and_b64 vcc, exec, s[4:5]
	s_cbranch_vccz .LBB6_81
	s_setprio 3
	s_load_dwordx2 s[8:9], s[0:1], 0x0
	s_load_dwordx2 s[10:11], s[0:1], 0x8
	s_load_dwordx2 s[12:13], s[0:1], 0x18
	s_load_dwordx2 s[32:33], s[0:1], 0x28
	s_load_dwordx4 s[36:39], s[0:1], 0x30
	s_load_dwordx2 s[18:19], s[0:1], 0xb8
	s_load_dwordx2 s[16:17], s[0:1], 0xc8
	s_load_dword s34, s[0:1], 0xd4
	s_lshr_b32 s3, s2, 4
	s_bfe_u32 s4, s2, 0x10003
	s_and_b32 s5, s2, 7
	v_lshrrev_b32_e32 v1, 6, v0
	v_and_b32_e32 v2, 63, v0
	v_and_b32_e32 v3, 15, v0
	v_bfe_u32 v4, v0, 4, 2
	s_nop 1
	v_readfirstlane_b32 s6, v1
	s_waitcnt lgkmcnt(0)
	s_cmp_eq_u32 s3, 0
	s_cselect_b32 s12, s12, s32
	s_cselect_b32 s13, s13, s33
	s_cselect_b32 s14, s36, s38
	s_cselect_b32 s15, s37, s39
	s_mul_i32 s35, s4, 0x708
	s_add_u32 s12, s12, s35
	s_addc_u32 s13, s13, 0
	s_mul_i32 s35, s5, 0x25800
	s_add_u32 s14, s14, s35
	s_addc_u32 s15, s15, 0
	s_mul_i32 s35, s4, 0x258
	s_add_u32 s14, s14, s35
	s_addc_u32 s15, s15, 0
	s_lshl_b64 s[10:11], s[10:11], 2
	s_mul_i32 s35, s3, 0x384000
	s_add_u32 s8, s8, s35
	s_addc_u32 s9, s9, 0
	s_mul_i32 s35, s5, 0x70800
	s_add_u32 s8, s8, s35
	s_addc_u32 s9, s9, 0
	s_mul_i32 s35, s4, 0x708
	s_add_u32 s8, s8, s35
	s_addc_u32 s9, s9, 0
	s_mul_i32 s35, s4, 112
	s_lshl_b32 s40, s6, 1
	s_add_i32 s35, s35, s40
	s_mul_i32 s35, s35, 0xe10
	s_add_u32 s22, s8, s35
	s_addc_u32 s23, s9, 0
	s_add_u32 s46, s22, 0xe10
	s_addc_u32 s47, s23, 0
	s_add_u32 s24, s22, s10
	s_addc_u32 s25, s23, s11
	s_add_u32 s48, s24, 0xe10
	s_addc_u32 s49, s25, 0
	s_cmp_eq_u32 s4, 0
	s_mov_b32 s27, 0xffff1f00
	s_mov_b32 s20, 0xfffffb50
	s_cselect_b32 s27, 0xe100, s27
	s_cselect_b32 s50, 0, -1
	s_cselect_b32 s20, 0x4b0, s20
	s_cselect_b32 s21, 0, -1
	s_lshl_b32 s35, s3, 1
	s_add_i32 s35, s35, s4
	s_add_i32 s35, s35, s34
	s_mul_i32 s35, s35, 0x28000
	s_add_u32 s16, s16, s35
	s_addc_u32 s17, s17, 0
	s_mul_i32 s35, s6, 0x5000
	s_add_u32 s16, s16, s35
	s_addc_u32 s17, s17, 0
	s_mov_b32 s28, 0xffff
	s_mov_b32 s29, 0
	s_mov_b32 s30, -1
	s_mov_b32 s31, 1
	s_mov_b32 s68, 0x00330033
	s_mov_b32 s69, 0x00330033
	s_mov_b32 s51, 0xbfb8aa3b
	s_mov_b32 s52, 0x4038aa3b
	v_lshlrev_b32_e32 v5, 4, v2
	v_mov_b32_e32 v36, 0
	v_mov_b32_e32 v37, 0
	v_mov_b32_e32 v38, 0
	v_mov_b32_e32 v39, 0
	v_mov_b32_e32 v60, 0
	v_mov_b32_e32 v61, 0
	v_mov_b32_e32 v62, 0
	v_mov_b32_e32 v63, 0
	v_mov_b32_e32 v84, 0
	v_mov_b32_e32 v85, 0
	v_mov_b32_e32 v86, 0
	v_mov_b32_e32 v87, 0
	v_mov_b32_e32 v108, 0
	v_mov_b32_e32 v109, 0
	v_mov_b32_e32 v110, 0
	v_mov_b32_e32 v111, 0
	s_add_u32 s42, s16, 0x0
	s_addc_u32 s43, s17, 0
	global_load_dwordx4 v[16:19], v5, s[42:43] offset:0
	global_load_dwordx4 v[20:23], v5, s[42:43] offset:1024
	global_load_dwordx4 v[24:27], v5, s[42:43] offset:2048
	global_load_dwordx4 v[28:31], v5, s[42:43] offset:3072
	s_add_u32 s42, s16, 0x1000
	s_addc_u32 s43, s17, 0
	global_load_dwordx4 v[32:35], v5, s[42:43]
	s_add_u32 s42, s16, 0x1400
	s_addc_u32 s43, s17, 0
	global_load_dwordx4 v[40:43], v5, s[42:43] offset:0
	global_load_dwordx4 v[44:47], v5, s[42:43] offset:1024
	global_load_dwordx4 v[48:51], v5, s[42:43] offset:2048
	global_load_dwordx4 v[52:55], v5, s[42:43] offset:3072
	s_add_u32 s42, s16, 0x2400
	s_addc_u32 s43, s17, 0
	global_load_dwordx4 v[56:59], v5, s[42:43]
	s_add_u32 s42, s16, 0x2800
	s_addc_u32 s43, s17, 0
	global_load_dwordx4 v[64:67], v5, s[42:43] offset:0
	global_load_dwordx4 v[68:71], v5, s[42:43] offset:1024
	global_load_dwordx4 v[72:75], v5, s[42:43] offset:2048
	global_load_dwordx4 v[76:79], v5, s[42:43] offset:3072
	s_add_u32 s42, s16, 0x3800
	s_addc_u32 s43, s17, 0
	global_load_dwordx4 v[80:83], v5, s[42:43]
	s_add_u32 s42, s16, 0x3c00
	s_addc_u32 s43, s17, 0
	global_load_dwordx4 v[88:91], v5, s[42:43] offset:0
	global_load_dwordx4 v[92:95], v5, s[42:43] offset:1024
	global_load_dwordx4 v[96:99], v5, s[42:43] offset:2048
	global_load_dwordx4 v[100:103], v5, s[42:43] offset:3072
	s_add_u32 s42, s16, 0x4c00
	s_addc_u32 s43, s17, 0
	global_load_dwordx4 v[104:107], v5, s[42:43]
	v_lshlrev_b32_e32 v172, 3, v2
	v_min_u32_e32 v6, 32, v2
	v_lshlrev_b32_e32 v114, 3, v6
	global_load_dwordx2 v[176:177], v172, s[22:23] offset:0
	global_load_dwordx2 v[178:179], v172, s[22:23] offset:512
	global_load_dwordx2 v[180:181], v172, s[22:23] offset:1024
	global_load_dwordx2 v[182:183], v114, s[22:23] offset:1536
	global_load_dwordx2 v[192:193], v172, s[24:25] offset:0
	global_load_dwordx2 v[194:195], v172, s[24:25] offset:512
	global_load_dwordx2 v[196:197], v172, s[24:25] offset:1024
	global_load_dwordx2 v[198:199], v114, s[24:25] offset:1536
	global_load_dwordx2 v[184:185], v172, s[46:47] offset:0
	global_load_dwordx2 v[186:187], v172, s[46:47] offset:512
	global_load_dwordx2 v[188:189], v172, s[46:47] offset:1024
	global_load_dwordx2 v[190:191], v114, s[46:47] offset:1536
	global_load_dwordx2 v[200:201], v172, s[48:49] offset:0
	global_load_dwordx2 v[202:203], v172, s[48:49] offset:512
	global_load_dwordx2 v[204:205], v172, s[48:49] offset:1024
	global_load_dwordx2 v[206:207], v114, s[48:49] offset:1536
	v_and_b32_e32 v6, 1, v3
	v_cmp_eq_u32_e32 vcc, 1, v6
	v_mov_b32_e32 v7, 0x44444444
	v_mov_b32_e32 v8, 0xeeeeeeee
	s_nop 1
	v_cndmask_b32_e32 v112, v7, v8, vcc
	s_mul_i32 s53, s6, 19
	v_add_u32_e32 v6, s53, v3
	v_cmp_gt_u32_e32 vcc, 0x96, v6
	v_add_u32_e32 v7, 0x12c, v6
	v_mov_b32_e32 v8, 0x12c
	s_nop 1
	v_cndmask_b32_e32 v7, v8, v7, vcc
	v_lshlrev_b32_e32 v7, 2, v7
	global_load_dword v9, v7, s[12:13]
	s_mov_b64 s[54:55], vcc
	v_cmp_gt_u32_e32 vcc, 0xc0, v0
	v_lshlrev_b32_e32 v10, 2, v0
	v_mov_b32_e32 v11, 0
	s_and_saveexec_b64 s[44:45], vcc
	ds_write_b32 v10, v11 offset:61440
	s_mov_b64 exec, s[44:45]
	v_and_b32_e32 v10, 31, v0
	v_lshrrev_b32_e32 v11, 5, v0
	v_subrev_u32_e32 v12, 6, v10
	v_max_i32_e32 v12, 0, v12
	v_mul_u32_u24_e32 v13, 11, v12
	v_lshrrev_b32_e32 v13, 5, v13
	v_mul_u32_u24_e32 v14, 3, v13
	v_sub_u32_e32 v14, v12, v14
	v_mul_u32_u24_e32 v15, 19, v13
	v_add3_u32 v15, v15, v14, 16
	v_cmp_gt_u32_e32 vcc, 0x96, v15
	v_cmp_lt_u32_e64 s[56:57], 5, v10
	v_cmp_gt_u32_e64 s[58:59], 30, v10
	s_and_b64 s[56:57], s[56:57], vcc
	s_and_b64 s[56:57], s[56:57], s[58:59]
	v_add_u32_e32 v15, 0x12c, v15
	v_mov_b32_e32 v14, 0x12c
	v_cndmask_b32_e64 v15, v14, v15, s[56:57]
	v_lshlrev_b32_e32 v15, 2, v15
	global_load_dword v14, v15, s[12:13]
	v_mul_u32_u24_e32 v11, 0x780, v11
	v_lshl_add_u32 v11, v10, 2, v11
	s_waitcnt vmcnt(0)
	v_mul_f32_e32 v14, s52, v14
	v_mul_f32_e32 v9, s52, v9
	v_cndmask_b32_e64 v14, 0, v14, s[56:57]
	v_cndmask_b32_e64 v113, 0, v9, s[54:55]
	s_and_saveexec_b64 s[44:45], s[58:59]
	ds_write_b32 v11, v14 offset:1800
	ds_write_b32 v11, v14 offset:32520
	s_mov_b64 exec, s[44:45]
	v_lshlrev_b32_e32 v172, 3, v2
	s_lshl_b32 s35, s6, 1
	s_sub_i32 s40, 15, s35
	s_cmp_eq_u32 s4, 0
	s_cselect_b32 s41, s35, s40
	s_add_i32 s35, s35, 1
	s_sub_i32 s40, 15, s35
	s_cmp_eq_u32 s4, 0
	s_cselect_b32 s40, s35, s40
	s_mul_i32 s41, s41, 0x780
	s_mul_i32 s40, s40, 0x780
	v_add_u32_e32 v173, s41, v172
	v_add_u32_e32 v174, s40, v172
	v_min_u32_e32 v6, 32, v2
	v_lshlrev_b32_e32 v114, 3, v6
	v_add_u32_e32 v115, s41, v114
	v_add_u32_e32 v169, s40, v114
	v_cmp_lt_u32_e32 vcc, 21, v2
	v_mov_b32_e32 v6, s51
	v_mov_b32_e32 v7, s52
	s_nop 0
	v_cndmask_b32_e32 v175, v6, v7, vcc
	s_waitcnt vmcnt(0)
	v_add_f32_e32 v176, v176, v192
	v_add_f32_e32 v177, v177, v193
	v_mul_f32_e32 v176, s51, v176
	v_mul_f32_e32 v177, s51, v177
	v_add_f32_e32 v178, v178, v194
	v_add_f32_e32 v179, v179, v195
	v_mul_f32_e32 v178, s51, v178
	v_mul_f32_e32 v179, s51, v179
	v_add_f32_e32 v180, v180, v196
	v_add_f32_e32 v181, v181, v197
	v_mul_f32_e32 v180, v175, v180
	v_mul_f32_e32 v181, v175, v181
	v_add_f32_e32 v182, v182, v198
	v_add_f32_e32 v183, v183, v199
	v_mul_f32_e32 v182, s52, v182
	v_mul_f32_e32 v183, s52, v183
	ds_write_b64 v173, v[176:177] offset:0
	ds_write_b64 v173, v[178:179] offset:512
	ds_write_b64 v173, v[180:181] offset:1024
	ds_write_b64 v115, v[182:183] offset:1536
	v_add_f32_e32 v184, v184, v200
	v_add_f32_e32 v185, v185, v201
	v_mul_f32_e32 v184, s51, v184
	v_mul_f32_e32 v185, s51, v185
	v_add_f32_e32 v186, v186, v202
	v_add_f32_e32 v187, v187, v203
	v_mul_f32_e32 v186, s51, v186
	v_mul_f32_e32 v187, s51, v187
	v_add_f32_e32 v188, v188, v204
	v_add_f32_e32 v189, v189, v205
	v_mul_f32_e32 v188, v175, v188
	v_mul_f32_e32 v189, v175, v189
	v_add_f32_e32 v190, v190, v206
	v_add_f32_e32 v191, v191, v207
	v_mul_f32_e32 v190, s52, v190
	v_mul_f32_e32 v191, s52, v191
	ds_write_b64 v174, v[184:185] offset:0
	ds_write_b64 v174, v[186:187] offset:512
	ds_write_b64 v174, v[188:189] offset:1024
	ds_write_b64 v169, v[190:191] offset:1536
	s_movk_i32 s55, 0x7800
	v_add_u32_e32 v173, s55, v173
	v_add_u32_e32 v174, s55, v174
	v_add_u32_e32 v115, s55, v115
	v_add_u32_e32 v169, s55, v169
	s_sub_i32 s55, 0, s55
	v_add_u32_e32 v6, s53, v2
	v_cmp_gt_u32_e32 vcc, 0x96, v6
	v_cmp_gt_u32_e64 s[56:57], 16, v2
	v_cmp_gt_u32_e64 s[58:59], 19, v2
	s_and_b64 s[56:57], s[56:57], vcc
	s_and_b64 s[58:59], s[58:59], vcc
	v_mov_b32_e32 v7, 0x710
	v_lshlrev_b32_e32 v8, 2, v6
	v_add_u32_e32 v9, 0x258, v8
	v_add_u32_e32 v10, 0x4b0, v8
	v_cndmask_b32_e64 v163, v7, v8, s[56:57]
	v_cndmask_b32_e64 v164, v7, v9, s[56:57]
	v_cndmask_b32_e64 v166, v7, v10, s[58:59]
	v_subrev_u32_e32 v9, 16, v2
	v_cmp_gt_u32_e64 s[60:61], 6, v9
	v_cmp_lt_u32_e32 vcc, 2, v9
	v_mov_b32_e32 v11, 0x93
	s_nop 0
	v_cndmask_b32_e32 v10, 0, v11, vcc
	v_cndmask_b32_e64 v12, 0, 3, vcc
	v_sub_u32_e32 v13, v6, v12
	v_cmp_gt_u32_e32 vcc, 0x96, v13
	s_and_b64 s[60:61], s[60:61], vcc
	v_add_u32_e32 v13, v6, v10
	v_lshlrev_b32_e32 v13, 2, v13
	v_cndmask_b32_e64 v165, v7, v13, s[60:61]
	v_subrev_u32_e32 v9, 22, v2
	v_cmp_gt_u32_e32 vcc, 3, v9
	s_mul_i32 s35, s6, 3
	s_addk_i32 s35, 0x1c8
	v_add_lshl_u32 v9, v9, s35, 2
	s_nop 0
	v_cndmask_b32_e32 v165, v165, v9, vcc
	v_and_b32_e32 v9, 1, v3
	v_lshlrev_b32_e32 v9, 4, v9
	v_lshl_or_b32 v9, v4, 5, v9
	v_add_u32_e32 v167, 0xf000, v9
	v_and_b32_e32 v9, 0xfffffff0, v6
	v_bfe_u32 v10, v6, 1, 1
	v_lshl_or_b32 v9, v10, 3, v9
	v_bfe_u32 v10, v6, 2, 2
	v_lshl_or_b32 v9, v10, 1, v9
	v_and_b32_e32 v10, 1, v6
	v_or_b32_e32 v9, v9, v10
	v_lshlrev_b32_e32 v9, 1, v9
	v_add_u32_e32 v9, 0xf000, v9
	v_lshlrev_b32_e32 v10, 1, v2
	v_add_u32_e32 v10, 0xf300, v10
	v_cndmask_b32_e64 v168, v10, v9, s[58:59]
	s_mul_i32 s35, s4, 0x25350
	s_add_u32 s14, s14, s35
	s_addc_u32 s15, s15, 0
	s_add_u32 s18, s18, 0x25800
	s_addc_u32 s19, s19, 0
	v_lshlrev_b32_e32 v9, 2, v0
	v_mov_b32_e32 v10, s18
	v_mov_b32_e32 v11, s19
	v_mov_b32_e32 v12, s14
	v_mov_b32_e32 v13, s15
	v_cndmask_b32_e64 v9, v9, v8, s[58:59]
	v_cndmask_b32_e64 v10, v10, v12, s[58:59]
	v_cndmask_b32_e64 v11, v11, v13, s[58:59]
	v_add_co_u32_e32 v170, vcc, v10, v9
	s_nop 1
	v_addc_co_u32_e32 v171, vcc, 0, v11, vcc
	v_mov_b32_e32 v161, 0
	v_mov_b32_e32 v137, 0
	v_mov_b32_e32 v138, 0
	v_mov_b32_e32 v139, 0
	v_mov_b32_e32 v141, 0
	v_mov_b32_e32 v142, 0
	v_mov_b32_e32 v143, 0
	v_mov_b32_e32 v145, 0
	v_mov_b32_e32 v146, 0
	v_mov_b32_e32 v147, 0
	v_mov_b32_e32 v149, 0
	v_mov_b32_e32 v150, 0
	v_mov_b32_e32 v151, 0
	s_mov_b32 s26, 0
	s_waitcnt vmcnt(0) lgkmcnt(0)
	s_barrier
	ds_read_b32 v136, v163 offset:0
	ds_read_b32 v140, v164 offset:0
	ds_read_b32 v148, v165 offset:0
	ds_read_b32 v152, v166 offset:0
	v_mov_b32_e32 v144, v113
	s_waitcnt lgkmcnt(0)
.Lgru2_chunk:
	ds_read_b128 v[116:119], v167 offset:0
	ds_read_b128 v[120:123], v167 offset:128
	ds_read_b128 v[124:127], v167 offset:256
	s_waitcnt lgkmcnt(2)
	v_smfmac_f32_16x16x64_f16 v[136:139], v[116:119], v[16:23], v112
	v_smfmac_f32_16x16x64_f16 v[148:151], v[116:119], v[88:95], v112
	s_waitcnt lgkmcnt(1)
	v_smfmac_f32_16x16x64_f16 v[136:139], v[120:123], v[24:31], v112
	v_smfmac_f32_16x16x64_f16 v[148:151], v[120:123], v[96:103], v112
	s_waitcnt lgkmcnt(0)
	v_smfmac_f32_16x16x64_f16 v[136:139], v[124:127], v[32:39], v112
	v_smfmac_f32_16x16x64_f16 v[148:151], v[124:127], v[104:111], v112
	v_smfmac_f32_16x16x64_f16 v[144:147], v[116:119], v[64:71], v112
	v_smfmac_f32_16x16x64_f16 v[140:143], v[116:119], v[40:47], v112
	v_smfmac_f32_16x16x64_f16 v[144:147], v[120:123], v[72:79], v112
	v_smfmac_f32_16x16x64_f16 v[140:143], v[120:123], v[48:55], v112
	s_nop 3
	v_add_f32_e32 v153, v136, v137
	v_add_f32_e32 v156, v148, v149
	v_smfmac_f32_16x16x64_f16 v[144:147], v[124:127], v[80:87], v112
	v_cndmask_b32_e64 v159, v156, v153, s[28:29]
	v_exp_f32_e32 v159, v159
	v_smfmac_f32_16x16x64_f16 v[140:143], v[124:127], v[56:63], v112
	v_mov_b32_dpp v157, v156 row_shl:3 row_mask:0xf bank_mask:0xf bound_ctrl:1
	v_mov_b32_dpp v158, v156 row_shl:6 row_mask:0xf bank_mask:0xf bound_ctrl:1
	v_add_f32_e32 v159, 1.0, v159
	v_rcp_f32_e32 v159, v159
	s_nop 0
	v_add_f32_e32 v155, v144, v145
	v_cndmask_b32_e64 v155, v158, v155, s[28:29]
	v_fmac_f32_e32 v152, v159, v155
	v_exp_f32_e32 v152, v152
	v_add_f32_e32 v154, v140, v141
	v_cndmask_b32_e64 v160, v157, v154, s[28:29]
	v_exp_f32_e32 v160, v160
	v_add_f32_e32 v152, 1.0, v152
	v_rcp_f32_e32 v159, v152
	v_add_f32_e32 v160, 1.0, v160
	v_rcp_f32_e32 v160, v160
	ds_read_b32 v136, v163 offset:1920
	ds_read_b32 v140, v164 offset:1920
	ds_read_b32 v148, v165 offset:1920
	v_mov_b32_e32 v144, v113
	v_fma_f32 v159, v159, -2.0, 1.0
	ds_read_b32 v152, v166 offset:1920
	v_sub_f32_e32 v153, v161, v159
	v_fma_mixlo_f16 v162, v160, v153, v159
	ds_write_b16 v168, v162 offset:384
	v_fma_f32 v161, v160, v153, v159
	v_mov_b32_e32 v137, 0
	v_mov_b32_e32 v141, 0
	v_mov_b32_e32 v145, 0
	v_mov_b32_e32 v149, 0
	global_store_dword v[170:171], v161, off
	v_lshl_add_u64 v[170:171], v[170:171], 0, s[20:21]
	s_waitcnt lgkmcnt(0)
	s_barrier
	ds_read_b128 v[116:119], v167 offset:384
	ds_read_b128 v[120:123], v167 offset:512
	ds_read_b128 v[124:127], v167 offset:640
	s_waitcnt lgkmcnt(2)
	v_smfmac_f32_16x16x64_f16 v[136:139], v[116:119], v[16:23], v112
	v_smfmac_f32_16x16x64_f16 v[148:151], v[116:119], v[88:95], v112
	s_waitcnt lgkmcnt(1)
	v_smfmac_f32_16x16x64_f16 v[136:139], v[120:123], v[24:31], v112
	v_smfmac_f32_16x16x64_f16 v[148:151], v[120:123], v[96:103], v112
	s_waitcnt lgkmcnt(0)
	v_smfmac_f32_16x16x64_f16 v[136:139], v[124:127], v[32:39], v112
	v_smfmac_f32_16x16x64_f16 v[148:151], v[124:127], v[104:111], v112
	s_cmp_eq_u32 s26, 7
	s_cbranch_scc1 .Lgru2_nopf
	s_add_u32 s22, s22, s27
	s_addc_u32 s23, s23, s50
	s_add_u32 s46, s46, s27
	s_addc_u32 s47, s47, s50
	s_add_u32 s24, s24, s27
	s_addc_u32 s25, s25, s50
	s_add_u32 s48, s48, s27
	s_addc_u32 s49, s49, s50
	global_load_dwordx2 v[176:177], v172, s[22:23] offset:0
	global_load_dwordx2 v[178:179], v172, s[22:23] offset:512
	global_load_dwordx2 v[180:181], v172, s[22:23] offset:1024
	global_load_dwordx2 v[192:193], v172, s[24:25] offset:0
	global_load_dwordx2 v[194:195], v172, s[24:25] offset:512
	global_load_dwordx2 v[196:197], v172, s[24:25] offset:1024
	global_load_dwordx2 v[184:185], v172, s[46:47] offset:0
	global_load_dwordx2 v[186:187], v172, s[46:47] offset:512
	global_load_dwordx2 v[188:189], v172, s[46:47] offset:1024
	global_load_dwordx2 v[200:201], v172, s[48:49] offset:0
	global_load_dwordx2 v[202:203], v172, s[48:49] offset:512
	global_load_dwordx2 v[204:205], v172, s[48:49] offset:1024
	global_load_dwordx2 v[182:183], v114, s[22:23] offset:1536
	global_load_dwordx2 v[198:199], v114, s[24:25] offset:1536
	global_load_dwordx2 v[190:191], v114, s[46:47] offset:1536
	global_load_dwordx2 v[206:207], v114, s[48:49] offset:1536
.Lgru2_nopf:
	v_smfmac_f32_16x16x64_f16 v[144:147], v[116:119], v[64:71], v112
	v_smfmac_f32_16x16x64_f16 v[140:143], v[116:119], v[40:47], v112
	v_smfmac_f32_16x16x64_f16 v[144:147], v[120:123], v[72:79], v112
	v_smfmac_f32_16x16x64_f16 v[140:143], v[120:123], v[48:55], v112
	s_nop 3
	v_add_f32_e32 v153, v136, v137
	v_add_f32_e32 v156, v148, v149
	v_smfmac_f32_16x16x64_f16 v[144:147], v[124:127], v[80:87], v112
	v_cndmask_b32_e64 v159, v156, v153, s[28:29]
	v_exp_f32_e32 v159, v159
	v_smfmac_f32_16x16x64_f16 v[140:143], v[124:127], v[56:63], v112
	v_mov_b32_dpp v157, v156 row_shl:3 row_mask:0xf bank_mask:0xf bound_ctrl:1
	v_mov_b32_dpp v158, v156 row_shl:6 row_mask:0xf bank_mask:0xf bound_ctrl:1
	v_add_f32_e32 v159, 1.0, v159
	v_rcp_f32_e32 v159, v159
	s_nop 0
	v_add_f32_e32 v155, v144, v145
	v_cndmask_b32_e64 v155, v158, v155, s[28:29]
	v_fmac_f32_e32 v152, v159, v155
	v_exp_f32_e32 v152, v152
	v_add_f32_e32 v154, v140, v141
	v_cndmask_b32_e64 v160, v157, v154, s[28:29]
	v_exp_f32_e32 v160, v160
	v_add_f32_e32 v152, 1.0, v152
	v_rcp_f32_e32 v159, v152
	v_add_f32_e32 v160, 1.0, v160
	v_rcp_f32_e32 v160, v160
	ds_read_b32 v136, v163 offset:3840
	ds_read_b32 v140, v164 offset:3840
	ds_read_b32 v148, v165 offset:3840
	v_mov_b32_e32 v144, v113
	v_fma_f32 v159, v159, -2.0, 1.0
	ds_read_b32 v152, v166 offset:3840
	v_sub_f32_e32 v153, v161, v159
	v_fma_mixlo_f16 v162, v160, v153, v159
	ds_write_b16 v168, v162 offset:0
	v_fma_f32 v161, v160, v153, v159
	v_mov_b32_e32 v137, 0
	v_mov_b32_e32 v141, 0
	v_mov_b32_e32 v145, 0
	v_mov_b32_e32 v149, 0
	global_store_dword v[170:171], v161, off
	v_lshl_add_u64 v[170:171], v[170:171], 0, s[20:21]
	s_waitcnt lgkmcnt(0)
	s_barrier
	ds_read_b128 v[116:119], v167 offset:0
	ds_read_b128 v[120:123], v167 offset:128
	ds_read_b128 v[124:127], v167 offset:256
	s_waitcnt lgkmcnt(2)
	v_smfmac_f32_16x16x64_f16 v[136:139], v[116:119], v[16:23], v112
	v_smfmac_f32_16x16x64_f16 v[148:151], v[116:119], v[88:95], v112
	s_waitcnt lgkmcnt(1)
	v_smfmac_f32_16x16x64_f16 v[136:139], v[120:123], v[24:31], v112
	v_smfmac_f32_16x16x64_f16 v[148:151], v[120:123], v[96:103], v112
	s_waitcnt lgkmcnt(0)
	v_smfmac_f32_16x16x64_f16 v[136:139], v[124:127], v[32:39], v112
	v_smfmac_f32_16x16x64_f16 v[148:151], v[124:127], v[104:111], v112
	v_smfmac_f32_16x16x64_f16 v[144:147], v[116:119], v[64:71], v112
	v_smfmac_f32_16x16x64_f16 v[140:143], v[116:119], v[40:47], v112
	v_smfmac_f32_16x16x64_f16 v[144:147], v[120:123], v[72:79], v112
	v_smfmac_f32_16x16x64_f16 v[140:143], v[120:123], v[48:55], v112
	s_nop 3
	v_add_f32_e32 v153, v136, v137
	v_add_f32_e32 v156, v148, v149
	v_smfmac_f32_16x16x64_f16 v[144:147], v[124:127], v[80:87], v112
	v_cndmask_b32_e64 v159, v156, v153, s[28:29]
	v_exp_f32_e32 v159, v159
	v_smfmac_f32_16x16x64_f16 v[140:143], v[124:127], v[56:63], v112
	v_mov_b32_dpp v157, v156 row_shl:3 row_mask:0xf bank_mask:0xf bound_ctrl:1
	v_mov_b32_dpp v158, v156 row_shl:6 row_mask:0xf bank_mask:0xf bound_ctrl:1
	v_add_f32_e32 v159, 1.0, v159
	v_rcp_f32_e32 v159, v159
	s_nop 0
	v_add_f32_e32 v155, v144, v145
	v_cndmask_b32_e64 v155, v158, v155, s[28:29]
	v_fmac_f32_e32 v152, v159, v155
	v_exp_f32_e32 v152, v152
	v_add_f32_e32 v154, v140, v141
	v_cndmask_b32_e64 v160, v157, v154, s[28:29]
	v_exp_f32_e32 v160, v160
	v_add_f32_e32 v152, 1.0, v152
	v_rcp_f32_e32 v159, v152
	v_add_f32_e32 v160, 1.0, v160
	v_rcp_f32_e32 v160, v160
	ds_read_b32 v136, v163 offset:5760
	ds_read_b32 v140, v164 offset:5760
	ds_read_b32 v148, v165 offset:5760
	v_mov_b32_e32 v144, v113
	v_fma_f32 v159, v159, -2.0, 1.0
	ds_read_b32 v152, v166 offset:5760
	v_sub_f32_e32 v153, v161, v159
	v_fma_mixlo_f16 v162, v160, v153, v159
	ds_write_b16 v168, v162 offset:384
	v_fma_f32 v161, v160, v153, v159
	v_mov_b32_e32 v137, 0
	v_mov_b32_e32 v141, 0
	v_mov_b32_e32 v145, 0
	v_mov_b32_e32 v149, 0
	global_store_dword v[170:171], v161, off
	v_lshl_add_u64 v[170:171], v[170:171], 0, s[20:21]
	s_waitcnt lgkmcnt(0)
	s_barrier
	ds_read_b128 v[116:119], v167 offset:384
	ds_read_b128 v[120:123], v167 offset:512
	ds_read_b128 v[124:127], v167 offset:640
	s_waitcnt lgkmcnt(2)
	v_smfmac_f32_16x16x64_f16 v[136:139], v[116:119], v[16:23], v112
	v_smfmac_f32_16x16x64_f16 v[148:151], v[116:119], v[88:95], v112
	s_waitcnt lgkmcnt(1)
	v_smfmac_f32_16x16x64_f16 v[136:139], v[120:123], v[24:31], v112
	v_smfmac_f32_16x16x64_f16 v[148:151], v[120:123], v[96:103], v112
	s_waitcnt lgkmcnt(0)
	v_smfmac_f32_16x16x64_f16 v[136:139], v[124:127], v[32:39], v112
	v_smfmac_f32_16x16x64_f16 v[148:151], v[124:127], v[104:111], v112
	v_smfmac_f32_16x16x64_f16 v[144:147], v[116:119], v[64:71], v112
	v_smfmac_f32_16x16x64_f16 v[140:143], v[116:119], v[40:47], v112
	v_smfmac_f32_16x16x64_f16 v[144:147], v[120:123], v[72:79], v112
	v_smfmac_f32_16x16x64_f16 v[140:143], v[120:123], v[48:55], v112
	s_nop 3
	v_add_f32_e32 v153, v136, v137
	v_add_f32_e32 v156, v148, v149
	v_smfmac_f32_16x16x64_f16 v[144:147], v[124:127], v[80:87], v112
	v_cndmask_b32_e64 v159, v156, v153, s[28:29]
	v_exp_f32_e32 v159, v159
	v_smfmac_f32_16x16x64_f16 v[140:143], v[124:127], v[56:63], v112
	v_mov_b32_dpp v157, v156 row_shl:3 row_mask:0xf bank_mask:0xf bound_ctrl:1
	v_mov_b32_dpp v158, v156 row_shl:6 row_mask:0xf bank_mask:0xf bound_ctrl:1
	v_add_f32_e32 v159, 1.0, v159
	v_rcp_f32_e32 v159, v159
	s_nop 0
	v_add_f32_e32 v155, v144, v145
	v_cndmask_b32_e64 v155, v158, v155, s[28:29]
	v_fmac_f32_e32 v152, v159, v155
	v_exp_f32_e32 v152, v152
	v_add_f32_e32 v154, v140, v141
	v_cndmask_b32_e64 v160, v157, v154, s[28:29]
	v_exp_f32_e32 v160, v160
	v_add_f32_e32 v152, 1.0, v152
	v_rcp_f32_e32 v159, v152
	v_add_f32_e32 v160, 1.0, v160
	v_rcp_f32_e32 v160, v160
	ds_read_b32 v136, v163 offset:7680
	ds_read_b32 v140, v164 offset:7680
	ds_read_b32 v148, v165 offset:7680
	v_mov_b32_e32 v144, v113
	v_fma_f32 v159, v159, -2.0, 1.0
	ds_read_b32 v152, v166 offset:7680
	v_sub_f32_e32 v153, v161, v159
	v_fma_mixlo_f16 v162, v160, v153, v159
	ds_write_b16 v168, v162 offset:0
	v_fma_f32 v161, v160, v153, v159
	v_mov_b32_e32 v137, 0
	v_mov_b32_e32 v141, 0
	v_mov_b32_e32 v145, 0
	v_mov_b32_e32 v149, 0
	global_store_dword v[170:171], v161, off
	v_lshl_add_u64 v[170:171], v[170:171], 0, s[20:21]
	s_waitcnt lgkmcnt(0)
	s_barrier
	ds_read_b128 v[116:119], v167 offset:0
	ds_read_b128 v[120:123], v167 offset:128
	ds_read_b128 v[124:127], v167 offset:256
	s_waitcnt lgkmcnt(2)
	v_smfmac_f32_16x16x64_f16 v[136:139], v[116:119], v[16:23], v112
	v_smfmac_f32_16x16x64_f16 v[148:151], v[116:119], v[88:95], v112
	s_waitcnt lgkmcnt(1)
	v_smfmac_f32_16x16x64_f16 v[136:139], v[120:123], v[24:31], v112
	v_smfmac_f32_16x16x64_f16 v[148:151], v[120:123], v[96:103], v112
	s_waitcnt lgkmcnt(0)
	v_smfmac_f32_16x16x64_f16 v[136:139], v[124:127], v[32:39], v112
	v_smfmac_f32_16x16x64_f16 v[148:151], v[124:127], v[104:111], v112
	v_smfmac_f32_16x16x64_f16 v[144:147], v[116:119], v[64:71], v112
	v_smfmac_f32_16x16x64_f16 v[140:143], v[116:119], v[40:47], v112
	v_smfmac_f32_16x16x64_f16 v[144:147], v[120:123], v[72:79], v112
	v_smfmac_f32_16x16x64_f16 v[140:143], v[120:123], v[48:55], v112
	s_nop 3
	v_add_f32_e32 v153, v136, v137
	v_add_f32_e32 v156, v148, v149
	v_smfmac_f32_16x16x64_f16 v[144:147], v[124:127], v[80:87], v112
	v_cndmask_b32_e64 v159, v156, v153, s[28:29]
	v_exp_f32_e32 v159, v159
	v_smfmac_f32_16x16x64_f16 v[140:143], v[124:127], v[56:63], v112
	v_mov_b32_dpp v157, v156 row_shl:3 row_mask:0xf bank_mask:0xf bound_ctrl:1
	v_mov_b32_dpp v158, v156 row_shl:6 row_mask:0xf bank_mask:0xf bound_ctrl:1
	v_add_f32_e32 v159, 1.0, v159
	v_rcp_f32_e32 v159, v159
	s_nop 0
	v_add_f32_e32 v155, v144, v145
	v_cndmask_b32_e64 v155, v158, v155, s[28:29]
	v_fmac_f32_e32 v152, v159, v155
	v_exp_f32_e32 v152, v152
	v_add_f32_e32 v154, v140, v141
	v_cndmask_b32_e64 v160, v157, v154, s[28:29]
	v_exp_f32_e32 v160, v160
	v_add_f32_e32 v152, 1.0, v152
	v_rcp_f32_e32 v159, v152
	v_add_f32_e32 v160, 1.0, v160
	v_rcp_f32_e32 v160, v160
	ds_read_b32 v136, v163 offset:9600
	ds_read_b32 v140, v164 offset:9600
	ds_read_b32 v148, v165 offset:9600
	v_mov_b32_e32 v144, v113
	v_fma_f32 v159, v159, -2.0, 1.0
	ds_read_b32 v152, v166 offset:9600
	v_sub_f32_e32 v153, v161, v159
	v_fma_mixlo_f16 v162, v160, v153, v159
	ds_write_b16 v168, v162 offset:384
	v_fma_f32 v161, v160, v153, v159
	v_mov_b32_e32 v137, 0
	v_mov_b32_e32 v141, 0
	v_mov_b32_e32 v145, 0
	v_mov_b32_e32 v149, 0
	global_store_dword v[170:171], v161, off
	v_lshl_add_u64 v[170:171], v[170:171], 0, s[20:21]
	s_waitcnt lgkmcnt(0)
	s_barrier
	ds_read_b128 v[116:119], v167 offset:384
	ds_read_b128 v[120:123], v167 offset:512
	ds_read_b128 v[124:127], v167 offset:640
	s_waitcnt lgkmcnt(2)
	v_smfmac_f32_16x16x64_f16 v[136:139], v[116:119], v[16:23], v112
	v_smfmac_f32_16x16x64_f16 v[148:151], v[116:119], v[88:95], v112
	s_waitcnt lgkmcnt(1)
	v_smfmac_f32_16x16x64_f16 v[136:139], v[120:123], v[24:31], v112
	v_smfmac_f32_16x16x64_f16 v[148:151], v[120:123], v[96:103], v112
	s_waitcnt lgkmcnt(0)
	v_smfmac_f32_16x16x64_f16 v[136:139], v[124:127], v[32:39], v112
	v_smfmac_f32_16x16x64_f16 v[148:151], v[124:127], v[104:111], v112
	v_smfmac_f32_16x16x64_f16 v[144:147], v[116:119], v[64:71], v112
	v_smfmac_f32_16x16x64_f16 v[140:143], v[116:119], v[40:47], v112
	v_smfmac_f32_16x16x64_f16 v[144:147], v[120:123], v[72:79], v112
	v_smfmac_f32_16x16x64_f16 v[140:143], v[120:123], v[48:55], v112
	s_nop 3
	v_add_f32_e32 v153, v136, v137
	v_add_f32_e32 v156, v148, v149
	v_smfmac_f32_16x16x64_f16 v[144:147], v[124:127], v[80:87], v112
	v_cndmask_b32_e64 v159, v156, v153, s[28:29]
	v_exp_f32_e32 v159, v159
	v_smfmac_f32_16x16x64_f16 v[140:143], v[124:127], v[56:63], v112
	v_mov_b32_dpp v157, v156 row_shl:3 row_mask:0xf bank_mask:0xf bound_ctrl:1
	v_mov_b32_dpp v158, v156 row_shl:6 row_mask:0xf bank_mask:0xf bound_ctrl:1
	v_add_f32_e32 v159, 1.0, v159
	v_rcp_f32_e32 v159, v159
	s_nop 0
	v_add_f32_e32 v155, v144, v145
	v_cndmask_b32_e64 v155, v158, v155, s[28:29]
	v_fmac_f32_e32 v152, v159, v155
	v_exp_f32_e32 v152, v152
	v_add_f32_e32 v154, v140, v141
	v_cndmask_b32_e64 v160, v157, v154, s[28:29]
	v_exp_f32_e32 v160, v160
	v_add_f32_e32 v152, 1.0, v152
	v_rcp_f32_e32 v159, v152
	v_add_f32_e32 v160, 1.0, v160
	v_rcp_f32_e32 v160, v160
	ds_read_b32 v136, v163 offset:11520
	ds_read_b32 v140, v164 offset:11520
	ds_read_b32 v148, v165 offset:11520
	v_mov_b32_e32 v144, v113
	v_fma_f32 v159, v159, -2.0, 1.0
	ds_read_b32 v152, v166 offset:11520
	v_sub_f32_e32 v153, v161, v159
	v_fma_mixlo_f16 v162, v160, v153, v159
	ds_write_b16 v168, v162 offset:0
	v_fma_f32 v161, v160, v153, v159
	v_mov_b32_e32 v137, 0
	v_mov_b32_e32 v141, 0
	v_mov_b32_e32 v145, 0
	v_mov_b32_e32 v149, 0
	global_store_dword v[170:171], v161, off
	v_lshl_add_u64 v[170:171], v[170:171], 0, s[20:21]
	s_waitcnt lgkmcnt(0)
	s_barrier
	ds_read_b128 v[116:119], v167 offset:0
	ds_read_b128 v[120:123], v167 offset:128
	ds_read_b128 v[124:127], v167 offset:256
	s_waitcnt lgkmcnt(2)
	v_smfmac_f32_16x16x64_f16 v[136:139], v[116:119], v[16:23], v112
	v_smfmac_f32_16x16x64_f16 v[148:151], v[116:119], v[88:95], v112
	s_waitcnt lgkmcnt(1)
	v_smfmac_f32_16x16x64_f16 v[136:139], v[120:123], v[24:31], v112
	v_smfmac_f32_16x16x64_f16 v[148:151], v[120:123], v[96:103], v112
	s_waitcnt lgkmcnt(0)
	v_smfmac_f32_16x16x64_f16 v[136:139], v[124:127], v[32:39], v112
	v_smfmac_f32_16x16x64_f16 v[148:151], v[124:127], v[104:111], v112
	v_smfmac_f32_16x16x64_f16 v[144:147], v[116:119], v[64:71], v112
	v_smfmac_f32_16x16x64_f16 v[140:143], v[116:119], v[40:47], v112
	v_smfmac_f32_16x16x64_f16 v[144:147], v[120:123], v[72:79], v112
	v_smfmac_f32_16x16x64_f16 v[140:143], v[120:123], v[48:55], v112
	s_nop 3
	v_add_f32_e32 v153, v136, v137
	v_add_f32_e32 v156, v148, v149
	v_smfmac_f32_16x16x64_f16 v[144:147], v[124:127], v[80:87], v112
	v_cndmask_b32_e64 v159, v156, v153, s[28:29]
	v_exp_f32_e32 v159, v159
	v_smfmac_f32_16x16x64_f16 v[140:143], v[124:127], v[56:63], v112
	v_mov_b32_dpp v157, v156 row_shl:3 row_mask:0xf bank_mask:0xf bound_ctrl:1
	v_mov_b32_dpp v158, v156 row_shl:6 row_mask:0xf bank_mask:0xf bound_ctrl:1
	v_add_f32_e32 v159, 1.0, v159
	v_rcp_f32_e32 v159, v159
	s_nop 0
	v_add_f32_e32 v155, v144, v145
	v_cndmask_b32_e64 v155, v158, v155, s[28:29]
	v_fmac_f32_e32 v152, v159, v155
	v_exp_f32_e32 v152, v152
	v_add_f32_e32 v154, v140, v141
	v_cndmask_b32_e64 v160, v157, v154, s[28:29]
	v_exp_f32_e32 v160, v160
	v_add_f32_e32 v152, 1.0, v152
	v_rcp_f32_e32 v159, v152
	v_add_f32_e32 v160, 1.0, v160
	v_rcp_f32_e32 v160, v160
	ds_read_b32 v136, v163 offset:13440
	ds_read_b32 v140, v164 offset:13440
	ds_read_b32 v148, v165 offset:13440
	v_mov_b32_e32 v144, v113
	v_fma_f32 v159, v159, -2.0, 1.0
	ds_read_b32 v152, v166 offset:13440
	v_sub_f32_e32 v153, v161, v159
	v_fma_mixlo_f16 v162, v160, v153, v159
	ds_write_b16 v168, v162 offset:384
	v_fma_f32 v161, v160, v153, v159
	v_mov_b32_e32 v137, 0
	v_mov_b32_e32 v141, 0
	v_mov_b32_e32 v145, 0
	v_mov_b32_e32 v149, 0
	global_store_dword v[170:171], v161, off
	v_lshl_add_u64 v[170:171], v[170:171], 0, s[20:21]
	s_waitcnt lgkmcnt(0)
	s_barrier
	ds_read_b128 v[116:119], v167 offset:384
	ds_read_b128 v[120:123], v167 offset:512
	ds_read_b128 v[124:127], v167 offset:640
	s_waitcnt lgkmcnt(2)
	v_smfmac_f32_16x16x64_f16 v[136:139], v[116:119], v[16:23], v112
	v_smfmac_f32_16x16x64_f16 v[148:151], v[116:119], v[88:95], v112
	s_waitcnt lgkmcnt(1)
	v_smfmac_f32_16x16x64_f16 v[136:139], v[120:123], v[24:31], v112
	v_smfmac_f32_16x16x64_f16 v[148:151], v[120:123], v[96:103], v112
	s_waitcnt lgkmcnt(0)
	v_smfmac_f32_16x16x64_f16 v[136:139], v[124:127], v[32:39], v112
	v_smfmac_f32_16x16x64_f16 v[148:151], v[124:127], v[104:111], v112
	v_smfmac_f32_16x16x64_f16 v[144:147], v[116:119], v[64:71], v112
	v_smfmac_f32_16x16x64_f16 v[140:143], v[116:119], v[40:47], v112
	v_smfmac_f32_16x16x64_f16 v[144:147], v[120:123], v[72:79], v112
	v_smfmac_f32_16x16x64_f16 v[140:143], v[120:123], v[48:55], v112
	s_nop 3
	v_add_f32_e32 v153, v136, v137
	v_add_f32_e32 v156, v148, v149
	v_smfmac_f32_16x16x64_f16 v[144:147], v[124:127], v[80:87], v112
	v_cndmask_b32_e64 v159, v156, v153, s[28:29]
	v_exp_f32_e32 v159, v159
	v_smfmac_f32_16x16x64_f16 v[140:143], v[124:127], v[56:63], v112
	v_mov_b32_dpp v157, v156 row_shl:3 row_mask:0xf bank_mask:0xf bound_ctrl:1
	v_mov_b32_dpp v158, v156 row_shl:6 row_mask:0xf bank_mask:0xf bound_ctrl:1
	v_add_f32_e32 v159, 1.0, v159
	v_rcp_f32_e32 v159, v159
	s_nop 0
	v_add_f32_e32 v155, v144, v145
	v_cndmask_b32_e64 v155, v158, v155, s[28:29]
	v_fmac_f32_e32 v152, v159, v155
	v_exp_f32_e32 v152, v152
	v_add_f32_e32 v154, v140, v141
	v_cndmask_b32_e64 v160, v157, v154, s[28:29]
	v_exp_f32_e32 v160, v160
	v_add_f32_e32 v152, 1.0, v152
	v_rcp_f32_e32 v159, v152
	v_add_f32_e32 v160, 1.0, v160
	v_rcp_f32_e32 v160, v160
	ds_read_b32 v136, v163 offset:15360
	ds_read_b32 v140, v164 offset:15360
	ds_read_b32 v148, v165 offset:15360
	v_mov_b32_e32 v144, v113
	v_fma_f32 v159, v159, -2.0, 1.0
	ds_read_b32 v152, v166 offset:15360
	v_sub_f32_e32 v153, v161, v159
	v_fma_mixlo_f16 v162, v160, v153, v159
	ds_write_b16 v168, v162 offset:0
	v_fma_f32 v161, v160, v153, v159
	v_mov_b32_e32 v137, 0
	v_mov_b32_e32 v141, 0
	v_mov_b32_e32 v145, 0
	v_mov_b32_e32 v149, 0
	global_store_dword v[170:171], v161, off
	v_lshl_add_u64 v[170:171], v[170:171], 0, s[20:21]
	s_waitcnt lgkmcnt(0)
	s_barrier
	ds_read_b128 v[116:119], v167 offset:0
	ds_read_b128 v[120:123], v167 offset:128
	ds_read_b128 v[124:127], v167 offset:256
	s_waitcnt lgkmcnt(2)
	v_smfmac_f32_16x16x64_f16 v[136:139], v[116:119], v[16:23], v112
	v_smfmac_f32_16x16x64_f16 v[148:151], v[116:119], v[88:95], v112
	s_waitcnt lgkmcnt(1)
	v_smfmac_f32_16x16x64_f16 v[136:139], v[120:123], v[24:31], v112
	v_smfmac_f32_16x16x64_f16 v[148:151], v[120:123], v[96:103], v112
	s_waitcnt lgkmcnt(0)
	v_smfmac_f32_16x16x64_f16 v[136:139], v[124:127], v[32:39], v112
	v_smfmac_f32_16x16x64_f16 v[148:151], v[124:127], v[104:111], v112
	v_smfmac_f32_16x16x64_f16 v[144:147], v[116:119], v[64:71], v112
	v_smfmac_f32_16x16x64_f16 v[140:143], v[116:119], v[40:47], v112
	v_smfmac_f32_16x16x64_f16 v[144:147], v[120:123], v[72:79], v112
	v_smfmac_f32_16x16x64_f16 v[140:143], v[120:123], v[48:55], v112
	s_nop 3
	v_add_f32_e32 v153, v136, v137
	v_add_f32_e32 v156, v148, v149
	v_smfmac_f32_16x16x64_f16 v[144:147], v[124:127], v[80:87], v112
	v_cndmask_b32_e64 v159, v156, v153, s[28:29]
	v_exp_f32_e32 v159, v159
	v_smfmac_f32_16x16x64_f16 v[140:143], v[124:127], v[56:63], v112
	v_mov_b32_dpp v157, v156 row_shl:3 row_mask:0xf bank_mask:0xf bound_ctrl:1
	v_mov_b32_dpp v158, v156 row_shl:6 row_mask:0xf bank_mask:0xf bound_ctrl:1
	v_add_f32_e32 v159, 1.0, v159
	v_rcp_f32_e32 v159, v159
	s_nop 0
	v_add_f32_e32 v155, v144, v145
	v_cndmask_b32_e64 v155, v158, v155, s[28:29]
	v_fmac_f32_e32 v152, v159, v155
	v_exp_f32_e32 v152, v152
	v_add_f32_e32 v154, v140, v141
	v_cndmask_b32_e64 v160, v157, v154, s[28:29]
	v_exp_f32_e32 v160, v160
	v_add_f32_e32 v152, 1.0, v152
	v_rcp_f32_e32 v159, v152
	v_add_f32_e32 v160, 1.0, v160
	v_rcp_f32_e32 v160, v160
	ds_read_b32 v136, v163 offset:17280
	ds_read_b32 v140, v164 offset:17280
	ds_read_b32 v148, v165 offset:17280
	v_mov_b32_e32 v144, v113
	v_fma_f32 v159, v159, -2.0, 1.0
	ds_read_b32 v152, v166 offset:17280
	v_sub_f32_e32 v153, v161, v159
	v_fma_mixlo_f16 v162, v160, v153, v159
	ds_write_b16 v168, v162 offset:384
	v_fma_f32 v161, v160, v153, v159
	v_mov_b32_e32 v137, 0
	v_mov_b32_e32 v141, 0
	v_mov_b32_e32 v145, 0
	v_mov_b32_e32 v149, 0
	global_store_dword v[170:171], v161, off
	v_lshl_add_u64 v[170:171], v[170:171], 0, s[20:21]
	s_waitcnt lgkmcnt(0)
	s_barrier
	ds_read_b128 v[116:119], v167 offset:384
	ds_read_b128 v[120:123], v167 offset:512
	ds_read_b128 v[124:127], v167 offset:640
	s_waitcnt lgkmcnt(2)
	v_smfmac_f32_16x16x64_f16 v[136:139], v[116:119], v[16:23], v112
	v_smfmac_f32_16x16x64_f16 v[148:151], v[116:119], v[88:95], v112
	s_waitcnt lgkmcnt(1)
	v_smfmac_f32_16x16x64_f16 v[136:139], v[120:123], v[24:31], v112
	v_smfmac_f32_16x16x64_f16 v[148:151], v[120:123], v[96:103], v112
	s_waitcnt lgkmcnt(0)
	v_smfmac_f32_16x16x64_f16 v[136:139], v[124:127], v[32:39], v112
	v_smfmac_f32_16x16x64_f16 v[148:151], v[124:127], v[104:111], v112
	s_cmp_eq_u32 s26, 7
	s_cbranch_scc1 .Lgru2_nost0
	s_waitcnt vmcnt(4)
	v_add_f32_e32 v176, v176, v192
	v_add_f32_e32 v177, v177, v193
	v_mul_f32_e32 v176, s51, v176
	v_mul_f32_e32 v177, s51, v177
	v_add_f32_e32 v178, v178, v194
	v_add_f32_e32 v179, v179, v195
	v_mul_f32_e32 v178, s51, v178
	v_mul_f32_e32 v179, s51, v179
	v_add_f32_e32 v180, v180, v196
	v_add_f32_e32 v181, v181, v197
	v_mul_f32_e32 v180, v175, v180
	v_mul_f32_e32 v181, v175, v181
	v_add_f32_e32 v182, v182, v198
	v_add_f32_e32 v183, v183, v199
	v_mul_f32_e32 v182, s52, v182
	v_mul_f32_e32 v183, s52, v183
	ds_write_b64 v173, v[176:177] offset:0
	ds_write_b64 v173, v[178:179] offset:512
	ds_write_b64 v173, v[180:181] offset:1024
	ds_write_b64 v115, v[182:183] offset:1536
.Lgru2_nost0:
	v_smfmac_f32_16x16x64_f16 v[144:147], v[116:119], v[64:71], v112
	v_smfmac_f32_16x16x64_f16 v[140:143], v[116:119], v[40:47], v112
	v_smfmac_f32_16x16x64_f16 v[144:147], v[120:123], v[72:79], v112
	v_smfmac_f32_16x16x64_f16 v[140:143], v[120:123], v[48:55], v112
	s_nop 3
	v_add_f32_e32 v153, v136, v137
	v_add_f32_e32 v156, v148, v149
	v_smfmac_f32_16x16x64_f16 v[144:147], v[124:127], v[80:87], v112
	v_cndmask_b32_e64 v159, v156, v153, s[28:29]
	v_exp_f32_e32 v159, v159
	v_smfmac_f32_16x16x64_f16 v[140:143], v[124:127], v[56:63], v112
	v_mov_b32_dpp v157, v156 row_shl:3 row_mask:0xf bank_mask:0xf bound_ctrl:1
	v_mov_b32_dpp v158, v156 row_shl:6 row_mask:0xf bank_mask:0xf bound_ctrl:1
	v_add_f32_e32 v159, 1.0, v159
	v_rcp_f32_e32 v159, v159
	s_nop 0
	v_add_f32_e32 v155, v144, v145
	v_cndmask_b32_e64 v155, v158, v155, s[28:29]
	v_fmac_f32_e32 v152, v159, v155
	v_exp_f32_e32 v152, v152
	v_add_f32_e32 v154, v140, v141
	v_cndmask_b32_e64 v160, v157, v154, s[28:29]
	v_exp_f32_e32 v160, v160
	v_add_f32_e32 v152, 1.0, v152
	v_rcp_f32_e32 v159, v152
	v_add_f32_e32 v160, 1.0, v160
	v_rcp_f32_e32 v160, v160
	ds_read_b32 v136, v163 offset:19200
	ds_read_b32 v140, v164 offset:19200
	ds_read_b32 v148, v165 offset:19200
	v_mov_b32_e32 v144, v113
	v_fma_f32 v159, v159, -2.0, 1.0
	ds_read_b32 v152, v166 offset:19200
	v_sub_f32_e32 v153, v161, v159
	v_fma_mixlo_f16 v162, v160, v153, v159
	ds_write_b16 v168, v162 offset:0
	v_fma_f32 v161, v160, v153, v159
	v_mov_b32_e32 v137, 0
	v_mov_b32_e32 v141, 0
	v_mov_b32_e32 v145, 0
	v_mov_b32_e32 v149, 0
	global_store_dword v[170:171], v161, off
	v_lshl_add_u64 v[170:171], v[170:171], 0, s[20:21]
	s_waitcnt lgkmcnt(0)
	s_barrier
	ds_read_b128 v[116:119], v167 offset:0
	ds_read_b128 v[120:123], v167 offset:128
	ds_read_b128 v[124:127], v167 offset:256
	s_waitcnt lgkmcnt(2)
	v_smfmac_f32_16x16x64_f16 v[136:139], v[116:119], v[16:23], v112
	v_smfmac_f32_16x16x64_f16 v[148:151], v[116:119], v[88:95], v112
	s_waitcnt lgkmcnt(1)
	v_smfmac_f32_16x16x64_f16 v[136:139], v[120:123], v[24:31], v112
	v_smfmac_f32_16x16x64_f16 v[148:151], v[120:123], v[96:103], v112
	s_waitcnt lgkmcnt(0)
	v_smfmac_f32_16x16x64_f16 v[136:139], v[124:127], v[32:39], v112
	v_smfmac_f32_16x16x64_f16 v[148:151], v[124:127], v[104:111], v112
	v_smfmac_f32_16x16x64_f16 v[144:147], v[116:119], v[64:71], v112
	v_smfmac_f32_16x16x64_f16 v[140:143], v[116:119], v[40:47], v112
	v_smfmac_f32_16x16x64_f16 v[144:147], v[120:123], v[72:79], v112
	v_smfmac_f32_16x16x64_f16 v[140:143], v[120:123], v[48:55], v112
	s_nop 3
	v_add_f32_e32 v153, v136, v137
	v_add_f32_e32 v156, v148, v149
	v_smfmac_f32_16x16x64_f16 v[144:147], v[124:127], v[80:87], v112
	v_cndmask_b32_e64 v159, v156, v153, s[28:29]
	v_exp_f32_e32 v159, v159
	v_smfmac_f32_16x16x64_f16 v[140:143], v[124:127], v[56:63], v112
	v_mov_b32_dpp v157, v156 row_shl:3 row_mask:0xf bank_mask:0xf bound_ctrl:1
	v_mov_b32_dpp v158, v156 row_shl:6 row_mask:0xf bank_mask:0xf bound_ctrl:1
	v_add_f32_e32 v159, 1.0, v159
	v_rcp_f32_e32 v159, v159
	s_nop 0
	v_add_f32_e32 v155, v144, v145
	v_cndmask_b32_e64 v155, v158, v155, s[28:29]
	v_fmac_f32_e32 v152, v159, v155
	v_exp_f32_e32 v152, v152
	v_add_f32_e32 v154, v140, v141
	v_cndmask_b32_e64 v160, v157, v154, s[28:29]
	v_exp_f32_e32 v160, v160
	v_add_f32_e32 v152, 1.0, v152
	v_rcp_f32_e32 v159, v152
	v_add_f32_e32 v160, 1.0, v160
	v_rcp_f32_e32 v160, v160
	ds_read_b32 v136, v163 offset:21120
	ds_read_b32 v140, v164 offset:21120
	ds_read_b32 v148, v165 offset:21120
	v_mov_b32_e32 v144, v113
	v_fma_f32 v159, v159, -2.0, 1.0
	ds_read_b32 v152, v166 offset:21120
	v_sub_f32_e32 v153, v161, v159
	v_fma_mixlo_f16 v162, v160, v153, v159
	ds_write_b16 v168, v162 offset:384
	v_fma_f32 v161, v160, v153, v159
	v_mov_b32_e32 v137, 0
	v_mov_b32_e32 v141, 0
	v_mov_b32_e32 v145, 0
	v_mov_b32_e32 v149, 0
	global_store_dword v[170:171], v161, off
	v_lshl_add_u64 v[170:171], v[170:171], 0, s[20:21]
	s_waitcnt lgkmcnt(0)
	s_barrier
	ds_read_b128 v[116:119], v167 offset:384
	ds_read_b128 v[120:123], v167 offset:512
	ds_read_b128 v[124:127], v167 offset:640
	s_waitcnt lgkmcnt(2)
	v_smfmac_f32_16x16x64_f16 v[136:139], v[116:119], v[16:23], v112
	v_smfmac_f32_16x16x64_f16 v[148:151], v[116:119], v[88:95], v112
	s_waitcnt lgkmcnt(1)
	v_smfmac_f32_16x16x64_f16 v[136:139], v[120:123], v[24:31], v112
	v_smfmac_f32_16x16x64_f16 v[148:151], v[120:123], v[96:103], v112
	s_waitcnt lgkmcnt(0)
	v_smfmac_f32_16x16x64_f16 v[136:139], v[124:127], v[32:39], v112
	v_smfmac_f32_16x16x64_f16 v[148:151], v[124:127], v[104:111], v112
	s_cmp_eq_u32 s26, 7
	s_cbranch_scc1 .Lgru2_nost1
	s_waitcnt vmcnt(4)
	v_add_f32_e32 v184, v184, v200
	v_add_f32_e32 v185, v185, v201
	v_mul_f32_e32 v184, s51, v184
	v_mul_f32_e32 v185, s51, v185
	v_add_f32_e32 v186, v186, v202
	v_add_f32_e32 v187, v187, v203
	v_mul_f32_e32 v186, s51, v186
	v_mul_f32_e32 v187, s51, v187
	v_add_f32_e32 v188, v188, v204
	v_add_f32_e32 v189, v189, v205
	v_mul_f32_e32 v188, v175, v188
	v_mul_f32_e32 v189, v175, v189
	v_add_f32_e32 v190, v190, v206
	v_add_f32_e32 v191, v191, v207
	v_mul_f32_e32 v190, s52, v190
	v_mul_f32_e32 v191, s52, v191
	ds_write_b64 v174, v[184:185] offset:0
	ds_write_b64 v174, v[186:187] offset:512
	ds_write_b64 v174, v[188:189] offset:1024
	ds_write_b64 v169, v[190:191] offset:1536
